# speedup vs baseline: 1.0309x; 1.0309x over previous
_ZN12_GLOBAL__N_113search_kernelEPKfS1_PhPf:
	s_load_dwordx2 s[8:9], s[0:1], 0x0
	s_load_dwordx2 s[4:5], s[0:1], 0x10
	s_movk_i32 s3, 0x90
	v_readfirstlane_b32 s10, v0
	v_cmp_gt_u32_e32 vcc, s3, v0
	s_and_saveexec_b64 s[6:7], vcc
	v_mov_b32_e32 v2, -1
	v_lshlrev_b32_e32 v1, 3, v0
	v_mov_b32_e32 v3, v2
	ds_write_b64 v1, v[2:3] offset:16384
	s_or_b64 exec, exec, s[6:7]
	s_waitcnt lgkmcnt(0)
	s_add_u32 s6, s4, 0x240000
	s_addc_u32 s7, s5, 0
	s_lshl_b32 s11, s2, 1
	s_and_b32 s14, s11, 14
	s_ashr_i32 s11, s2, 7
	s_lshr_b32 s15, s10, 6
	s_add_i32 s14, s14, s11
	s_bfe_u32 s2, s2, 0x40003
	s_mul_i32 s11, s15, 24
	v_mul_u32_u24_e32 v2, 0x71d, v0
	v_mul_u32_u24_e32 v4, 0x195, v0
	s_min_u32 s18, s11, 0xa5
	s_mul_i32 s11, s14, 3
	s_mul_i32 s12, s2, 9
	s_mov_b32 s13, 0
	v_lshrrev_b32_e32 v3, 16, v2
	s_movk_i32 s19, 0xffdc
	v_lshrrev_b32_e32 v5, 17, v4
	v_mad_i32_i24 v2, v3, s19, v0
	v_mad_i32_i24 v4, v5, -9, v3
	v_add_u32_e32 v3, s11, v5
	v_mov_b64_e32 v[6:7], s[12:13]
	v_mad_i64_i32 v[8:9], s[16:17], v3, s3, v[6:7]
	v_ashrrev_i32_e32 v5, 31, v4
	v_lshl_add_u64 v[4:5], v[8:9], 0, v[4:5]
	s_movk_i32 s13, 0x240
	v_mov_b64_e32 v[8:9], s[8:9]
	v_mad_u64_u32 v[10:11], s[8:9], v4, s13, v[8:9]
	v_min_u32_e32 v4, 0x1cb, v0
	v_or_b32_e32 v4, 0x200, v4
	v_mad_i32_i24 v11, v5, s13, v11
	v_mul_u32_u24_e32 v5, 0x71d, v4
	v_ashrrev_i32_e32 v3, 31, v2
	v_lshrrev_b32_e32 v5, 16, v5
	v_lshl_add_u64 v[2:3], v[2:3], 4, v[10:11]
	v_mad_i32_i24 v10, v5, s19, v4
	v_mul_u32_u24_e32 v4, 0x653, v4
	v_lshrrev_b32_e32 v11, 19, v4
	v_mad_i32_i24 v4, v11, -9, v5
	v_add_u32_e32 v5, s11, v11
	v_mad_i64_i32 v[6:7], s[8:9], v5, s3, v[6:7]
	v_ashrrev_i32_e32 v5, 31, v4
	v_lshl_add_u64 v[4:5], v[6:7], 0, v[4:5]
	v_mad_u64_u32 v[12:13], s[8:9], v4, s13, v[8:9]
	s_mul_i32 s8, s14, 0x90
	s_barrier
	s_load_dwordx2 s[42:43], s[0:1], 0x8
	s_load_dwordx2 s[62:63], s[0:1], 0x0
	v_mov_b32_e32 v244, v2
	v_mov_b32_e32 v245, v3
	global_load_dwordx4 v[6:9], v[2:3], off
	v_mad_i32_i24 v13, v5, s13, v13
	v_ashrrev_i32_e32 v11, 31, v10
	v_lshl_add_u64 v[10:11], v[10:11], 4, v[12:13]
	v_mov_b32_e32 v246, v10
	v_mov_b32_e32 v247, v11
	global_load_dwordx4 v[10:13], v[10:11], off
	v_and_b32_e32 v1, 63, v0
	s_add_i32 s20, s8, s12
	s_lshl_b32 s20, s20, 10
	v_lshl_add_u32 v164, v1, 4, s20
	s_mul_i32 s9, s14, 0xbd
	s_add_i32 s21, s9, s18
	s_lshl_b32 s21, s21, 10
	v_lshl_add_u32 v165, v1, 4, s21
	s_add_u32 s22, s4, 0x1000
	s_addc_u32 s23, s5, 0
	s_add_u32 s24, s4, 0x2000
	s_addc_u32 s25, s5, 0
	s_mov_b32 s26, s6
	s_mov_b32 s27, s7
	s_add_u32 s28, s6, 0x1000
	s_addc_u32 s29, s7, 0
	s_add_u32 s30, s6, 0x2000
	s_addc_u32 s31, s7, 0
	s_add_u32 s32, s6, 0x3000
	s_addc_u32 s33, s7, 0
	s_add_u32 s34, s6, 0x4000
	s_addc_u32 s35, s7, 0
	s_add_u32 s36, s6, 0x5000
	s_addc_u32 s37, s7, 0
	v_bfe_u32 v166, v0, 4, 2
	v_and_b32_e32 v167, 15, v0
	v_lshlrev_b32_e32 v167, 3, v167
	s_mul_i32 s40, s15, 6
	s_mov_b32 s41, 0x7f000000
	global_load_dwordx4 v[112:115], v164, s[4:5]
	global_load_dwordx4 v[16:19], v165, s[26:27] nt
	global_load_dwordx4 v[20:23], v165, s[26:27] offset:1024 nt
	global_load_dwordx4 v[24:27], v165, s[26:27] offset:2048 nt
	global_load_dwordx4 v[28:31], v165, s[26:27] offset:3072 nt
	global_load_dwordx4 v[32:35], v165, s[28:29] nt
	global_load_dwordx4 v[36:39], v165, s[28:29] offset:1024 nt
	global_load_dwordx4 v[40:43], v165, s[28:29] offset:2048 nt
	global_load_dwordx4 v[44:47], v165, s[28:29] offset:3072 nt
	global_load_dwordx4 v[48:51], v165, s[30:31] nt
	global_load_dwordx4 v[52:55], v165, s[30:31] offset:1024 nt
	global_load_dwordx4 v[56:59], v165, s[30:31] offset:2048 nt
	global_load_dwordx4 v[60:63], v165, s[30:31] offset:3072 nt
	global_load_dwordx4 v[64:67], v165, s[32:33] nt
	global_load_dwordx4 v[68:71], v165, s[32:33] offset:1024 nt
	global_load_dwordx4 v[72:75], v165, s[32:33] offset:2048 nt
	global_load_dwordx4 v[76:79], v165, s[32:33] offset:3072 nt
	global_load_dwordx4 v[80:83], v165, s[34:35] nt
	global_load_dwordx4 v[84:87], v165, s[34:35] offset:1024 nt
	global_load_dwordx4 v[88:91], v165, s[34:35] offset:2048 nt
	global_load_dwordx4 v[92:95], v165, s[34:35] offset:3072 nt
	global_load_dwordx4 v[96:99], v165, s[36:37] nt
	global_load_dwordx4 v[100:103], v165, s[36:37] offset:1024 nt
	global_load_dwordx4 v[104:107], v165, s[36:37] offset:2048 nt
	global_load_dwordx4 v[108:111], v165, s[36:37] offset:3072 nt
	global_load_dwordx4 v[116:119], v164, s[4:5] offset:1024
	v_lshlrev_b32_e32 v14, 4, v0
	s_lshr_b32 s50, s15, 1
	s_and_b32 s51, s15, 1
	s_lshl_b32 s51, s51, 3
	s_mov_b32 s48, 0x1010101
	s_mov_b32 s49, 0x1010101
	s_movk_i32 s58, 0x900
	s_movk_i32 s59, 0xb40
	v_and_b32_e32 v168, 7, v0
	v_lshrrev_b32_e32 v177, 3, v1
	v_or_b32_e32 v177, s51, v177
	v_lshlrev_b32_e32 v169, 3, v177
	v_and_b32_e32 v179, 3, v0
	v_lshlrev_b32_e32 v179, 8, v179
	v_lshl_add_u32 v170, v177, 4, v179
	v_add_u32_e32 v170, s20, v170
	v_lshrrev_b32_e32 v179, 2, v168
	v_and_b32_e32 v180, 3, v0
	v_lshl_or_b32 v171, v179, 4, v180
	v_mul_u32_u24_e32 v179, 11, v168
	v_lshrrev_b32_e32 v179, 5, v179
	v_mul_u32_u24_e32 v180, 3, v179
	v_sub_u32_e32 v180, v168, v180
	v_mul_u32_u24_e32 v181, 0x90, v179
	v_add_u32_e32 v181, v181, v180
	v_mul_u32_u24_e32 v172, 0x240, v181
	v_mul_u32_u24_e32 v181, 0x48, v179
	v_add_u32_e32 v181, v181, v180
	v_mul_u32_u24_e32 v173, 0x120, v181
	v_mul_u32_u24_e32 v181, 0x24, v179
	v_add_u32_e32 v181, v181, v180
	v_mul_u32_u24_e32 v174, 0x90, v181
	v_mul_u32_u24_e32 v181, 9, v179
	v_add_u32_e32 v181, v181, v180
	v_mul_u32_u24_e32 v175, 0x240, v181
	v_add_u32_e32 v176, 8, v168
	s_waitcnt lgkmcnt(0)
	s_mul_i32 s60, s14, 0x3cc00
	s_add_u32 s42, s42, s60
	s_addc_u32 s43, s43, 0
	s_mul_i32 s60, s14, 0xf300
	s_add_u32 s44, s4, s60
	s_addc_u32 s45, s5, 0
	s_add_u32 s44, s44, 0x534000
	s_addc_u32 s45, s45, 0
	s_mul_i32 s60, s14, 0x3cc0
	s_add_u32 s46, s4, s60
	s_addc_u32 s47, s5, 0
	s_add_u32 s46, s46, 0x627000
	s_addc_u32 s47, s47, 0
	v_mov_b32_e32 v152, s42
	v_mov_b32_e32 v153, s43
	v_mov_b32_e32 v154, s44
	v_mov_b32_e32 v155, s45
	v_mov_b32_e32 v159, s46
	v_mov_b32_e32 v161, s47
	s_sub_u32 s60, s42, s62
	s_subb_u32 s61, s43, s63
	s_mul_i32 s62, s14, 0x3cc00
	s_sub_u32 s60, s60, s62
	s_subb_u32 s61, s61, 0
	v_lshl_add_u64 v[244:245], v[244:245], 0, s[60:61]
	v_lshl_add_u64 v[246:247], v[246:247], 0, s[60:61]
	s_lshl_b32 s62, s15, 10
	s_add_i32 s62, s62, 0x46e0
	s_mov_b32 m0, s62
	s_mul_i32 s62, s2, 0xf30
	s_add_u32 s60, s44, s62
	s_addc_u32 s61, s45, 0
	v_lshlrev_b32_e32 v240, 4, v0
	v_mov_b32_e32 v241, 0
	v_lshl_add_u64 v[240:241], v[240:241], 0, s[60:61]
	s_mul_i32 s62, s2, 0x3cc
	s_add_u32 s60, s46, s62
	s_addc_u32 s61, s47, 0
	v_lshlrev_b32_e32 v242, 2, v0
	v_mov_b32_e32 v243, 0
	v_lshl_add_u64 v[242:243], v[242:243], 0, s[60:61]
	global_load_lds_dwordx4 v[244:245], off
	global_load_lds_dwordx4 v[246:247], off
	global_load_lds_dwordx4 v[240:241], off
	global_load_lds_dword v[242:243], off
	s_waitcnt vmcnt(25)
	ds_write_b128 v14, v[6:9]
	ds_write_b128 v14, v[10:13] offset:8192
	v_mfma_f32_16x16x32_f16 v[120:123], v[16:19], v[112:115], 0
	v_mfma_f32_16x16x32_f16 v[124:127], v[20:23], v[112:115], 0
	v_mfma_f32_16x16x32_f16 v[128:131], v[24:27], v[112:115], 0
	v_mfma_f32_16x16x32_f16 v[132:135], v[28:31], v[112:115], 0
	s_waitcnt vmcnt(21)
	v_mfma_f32_16x16x32_f16 v[136:139], v[32:35], v[112:115], 0
	v_mfma_f32_16x16x32_f16 v[140:143], v[36:39], v[112:115], 0
	v_mfma_f32_16x16x32_f16 v[144:147], v[40:43], v[112:115], 0
	v_mfma_f32_16x16x32_f16 v[148:151], v[44:47], v[112:115], 0
	v_min3_i32 v160, v120, v121, s41
	v_min3_i32 v160, v122, v123, v160
	v_min3_i32 v160, v124, v125, v160
	v_min3_i32 v160, v126, v127, v160
	v_min3_i32 v160, v128, v129, v160
	v_min3_i32 v160, v130, v131, v160
	v_min3_i32 v160, v132, v133, v160
	v_min3_i32 v157, v134, v135, v160
	v_mov_b32_e32 v6, 0
	v_mov_b32_e32 v7, 0x900
	v_mov_b32_e32 v8, 0x240
	s_waitcnt vmcnt(17)
	v_mfma_f32_16x16x32_f16 v[120:123], v[48:51], v[112:115], 0
	v_mfma_f32_16x16x32_f16 v[124:127], v[52:55], v[112:115], 0
	v_mov_b32_e32 v158, 0
	v_mfma_f32_16x16x32_f16 v[128:131], v[56:59], v[112:115], 0
	v_mfma_f32_16x16x32_f16 v[132:135], v[60:63], v[112:115], 0
	v_min3_i32 v160, v136, v137, v157
	v_min3_i32 v160, v138, v139, v160
	v_min3_i32 v160, v140, v141, v160
	v_min3_i32 v160, v142, v143, v160
	v_min3_i32 v160, v144, v145, v160
	v_min3_i32 v160, v146, v147, v160
	v_min3_i32 v160, v148, v149, v160
	v_min3_i32 v156, v150, v151, v160
	v_cmp_ge_i32_e32 vcc, v156, v157
	s_waitcnt vmcnt(13)
	v_mfma_f32_16x16x32_f16 v[136:139], v[64:67], v[112:115], 0
	v_mfma_f32_16x16x32_f16 v[140:143], v[68:71], v[112:115], 0
	v_cndmask_b32_e32 v158, 1, v158, vcc
	v_mfma_f32_16x16x32_f16 v[144:147], v[72:75], v[112:115], 0
	v_mfma_f32_16x16x32_f16 v[148:151], v[76:79], v[112:115], 0
	v_min3_i32 v160, v120, v121, v156
	v_min3_i32 v160, v122, v123, v160
	v_min3_i32 v160, v124, v125, v160
	v_min3_i32 v160, v126, v127, v160
	v_min3_i32 v160, v128, v129, v160
	v_min3_i32 v160, v130, v131, v160
	v_min3_i32 v160, v132, v133, v160
	v_min3_i32 v157, v134, v135, v160
	v_cmp_ge_i32_e32 vcc, v157, v156
	s_waitcnt vmcnt(9)
	v_mfma_f32_16x16x32_f16 v[120:123], v[80:83], v[112:115], 0
	v_mfma_f32_16x16x32_f16 v[124:127], v[84:87], v[112:115], 0
	v_cndmask_b32_e32 v158, 2, v158, vcc
	v_mfma_f32_16x16x32_f16 v[128:131], v[88:91], v[112:115], 0
	v_mfma_f32_16x16x32_f16 v[132:135], v[92:95], v[112:115], 0
	v_min3_i32 v160, v136, v137, v157
	v_min3_i32 v160, v138, v139, v160
	v_min3_i32 v160, v140, v141, v160
	v_min3_i32 v160, v142, v143, v160
	v_min3_i32 v160, v144, v145, v160
	v_min3_i32 v160, v146, v147, v160
	v_min3_i32 v160, v148, v149, v160
	v_min3_i32 v156, v150, v151, v160
	v_cmp_ge_i32_e32 vcc, v156, v157
	s_waitcnt vmcnt(5)
	v_mfma_f32_16x16x32_f16 v[136:139], v[96:99], v[112:115], 0
	v_mfma_f32_16x16x32_f16 v[140:143], v[100:103], v[112:115], 0
	v_cndmask_b32_e32 v158, 3, v158, vcc
	v_mfma_f32_16x16x32_f16 v[144:147], v[104:107], v[112:115], 0
	v_mfma_f32_16x16x32_f16 v[148:151], v[108:111], v[112:115], 0
	v_min3_i32 v160, v120, v121, v156
	v_min3_i32 v160, v122, v123, v160
	v_min3_i32 v160, v124, v125, v160
	v_min3_i32 v160, v126, v127, v160
	v_min3_i32 v160, v128, v129, v160
	v_min3_i32 v160, v130, v131, v160
	v_min3_i32 v160, v132, v133, v160
	v_min3_i32 v157, v134, v135, v160
	v_cmp_ge_i32_e32 vcc, v157, v156
	s_waitcnt vmcnt(4)
	global_load_dwordx4 v[112:115], v164, s[4:5] offset:2048
	v_mfma_f32_16x16x32_f16 v[120:123], v[16:19], v[116:119], 0
	v_mfma_f32_16x16x32_f16 v[124:127], v[20:23], v[116:119], 0
	v_cndmask_b32_e32 v158, 4, v158, vcc
	v_mfma_f32_16x16x32_f16 v[128:131], v[24:27], v[116:119], 0
	v_mfma_f32_16x16x32_f16 v[132:135], v[28:31], v[116:119], 0
	v_min3_i32 v160, v136, v137, v157
	v_min3_i32 v160, v138, v139, v160
	v_min3_i32 v160, v140, v141, v160
	v_min3_i32 v160, v142, v143, v160
	v_min3_i32 v160, v144, v145, v160
	v_min3_i32 v160, v146, v147, v160
	v_min3_i32 v160, v148, v149, v160
	v_min3_i32 v156, v150, v151, v160
	v_cmp_ge_i32_e32 vcc, v156, v157
	v_mfma_f32_16x16x32_f16 v[136:139], v[32:35], v[116:119], 0
	v_mfma_f32_16x16x32_f16 v[140:143], v[36:39], v[116:119], 0
	v_cndmask_b32_e32 v158, 5, v158, vcc
	v_add_u32_e32 v162, s40, v158
	v_lshl_or_b32 v162, v162, 2, v166
	v_mov_b32_e32 v163, v156
	ds_min_u64 v167, v[162:163] offset:16384
	v_mfma_f32_16x16x32_f16 v[144:147], v[40:43], v[116:119], 0
	v_mfma_f32_16x16x32_f16 v[148:151], v[44:47], v[116:119], 0
	v_min3_i32 v160, v120, v121, s41
	v_min3_i32 v160, v122, v123, v160
	v_min3_i32 v160, v124, v125, v160
	v_min3_i32 v160, v126, v127, v160
	v_min3_i32 v160, v128, v129, v160
	v_min3_i32 v160, v130, v131, v160
	v_min3_i32 v160, v132, v133, v160
	v_min3_i32 v157, v134, v135, v160
	v_mfma_f32_16x16x32_f16 v[120:123], v[48:51], v[116:119], 0
	v_mfma_f32_16x16x32_f16 v[124:127], v[52:55], v[116:119], 0
	v_mov_b32_e32 v158, 0
	v_mfma_f32_16x16x32_f16 v[128:131], v[56:59], v[116:119], 0
	v_mfma_f32_16x16x32_f16 v[132:135], v[60:63], v[116:119], 0
	v_min3_i32 v160, v136, v137, v157
	v_min3_i32 v160, v138, v139, v160
	v_min3_i32 v160, v140, v141, v160
	v_min3_i32 v160, v142, v143, v160
	v_min3_i32 v160, v144, v145, v160
	v_min3_i32 v160, v146, v147, v160
	v_min3_i32 v160, v148, v149, v160
	v_min3_i32 v156, v150, v151, v160
	v_cmp_ge_i32_e32 vcc, v156, v157
	v_mfma_f32_16x16x32_f16 v[136:139], v[64:67], v[116:119], 0
	v_mfma_f32_16x16x32_f16 v[140:143], v[68:71], v[116:119], 0
	v_cndmask_b32_e32 v158, 1, v158, vcc
	v_mfma_f32_16x16x32_f16 v[144:147], v[72:75], v[116:119], 0
	v_mfma_f32_16x16x32_f16 v[148:151], v[76:79], v[116:119], 0
	v_min3_i32 v160, v120, v121, v156
	v_min3_i32 v160, v122, v123, v160
	v_min3_i32 v160, v124, v125, v160
	v_min3_i32 v160, v126, v127, v160
	v_min3_i32 v160, v128, v129, v160
	v_min3_i32 v160, v130, v131, v160
	v_min3_i32 v160, v132, v133, v160
	v_min3_i32 v157, v134, v135, v160
	v_cmp_ge_i32_e32 vcc, v157, v156
	v_mfma_f32_16x16x32_f16 v[120:123], v[80:83], v[116:119], 0
	v_mfma_f32_16x16x32_f16 v[124:127], v[84:87], v[116:119], 0
	v_cndmask_b32_e32 v158, 2, v158, vcc
	v_mfma_f32_16x16x32_f16 v[128:131], v[88:91], v[116:119], 0
	v_mfma_f32_16x16x32_f16 v[132:135], v[92:95], v[116:119], 0
	v_min3_i32 v160, v136, v137, v157
	v_min3_i32 v160, v138, v139, v160
	v_min3_i32 v160, v140, v141, v160
	v_min3_i32 v160, v142, v143, v160
	v_min3_i32 v160, v144, v145, v160
	v_min3_i32 v160, v146, v147, v160
	v_min3_i32 v160, v148, v149, v160
	v_min3_i32 v156, v150, v151, v160
	v_cmp_ge_i32_e32 vcc, v156, v157
	v_mfma_f32_16x16x32_f16 v[136:139], v[96:99], v[116:119], 0
	v_mfma_f32_16x16x32_f16 v[140:143], v[100:103], v[116:119], 0
	v_cndmask_b32_e32 v158, 3, v158, vcc
	v_mfma_f32_16x16x32_f16 v[144:147], v[104:107], v[116:119], 0
	v_mfma_f32_16x16x32_f16 v[148:151], v[108:111], v[116:119], 0
	v_min3_i32 v160, v120, v121, v156
	v_min3_i32 v160, v122, v123, v160
	v_min3_i32 v160, v124, v125, v160
	v_min3_i32 v160, v126, v127, v160
	v_min3_i32 v160, v128, v129, v160
	v_min3_i32 v160, v130, v131, v160
	v_min3_i32 v160, v132, v133, v160
	v_min3_i32 v157, v134, v135, v160
	v_cmp_ge_i32_e32 vcc, v157, v156
	s_waitcnt vmcnt(0)
	global_load_dwordx4 v[116:119], v164, s[4:5] offset:3072
	v_mfma_f32_16x16x32_f16 v[120:123], v[16:19], v[112:115], 0
	v_mfma_f32_16x16x32_f16 v[124:127], v[20:23], v[112:115], 0
	v_cndmask_b32_e32 v158, 4, v158, vcc
	v_mfma_f32_16x16x32_f16 v[128:131], v[24:27], v[112:115], 0
	v_mfma_f32_16x16x32_f16 v[132:135], v[28:31], v[112:115], 0
	v_min3_i32 v160, v136, v137, v157
	v_min3_i32 v160, v138, v139, v160
	v_min3_i32 v160, v140, v141, v160
	v_min3_i32 v160, v142, v143, v160
	v_min3_i32 v160, v144, v145, v160
	v_min3_i32 v160, v146, v147, v160
	v_min3_i32 v160, v148, v149, v160
	v_min3_i32 v156, v150, v151, v160
	v_cmp_ge_i32_e32 vcc, v156, v157
	v_mfma_f32_16x16x32_f16 v[136:139], v[32:35], v[112:115], 0
	v_mfma_f32_16x16x32_f16 v[140:143], v[36:39], v[112:115], 0
	v_cndmask_b32_e32 v158, 5, v158, vcc
	v_add_u32_e32 v162, s40, v158
	v_lshl_or_b32 v162, v162, 2, v166
	v_mov_b32_e32 v163, v156
	ds_min_u64 v167, v[162:163] offset:16512
	v_mfma_f32_16x16x32_f16 v[144:147], v[40:43], v[112:115], 0
	v_mfma_f32_16x16x32_f16 v[148:151], v[44:47], v[112:115], 0
	v_min3_i32 v160, v120, v121, s41
	v_min3_i32 v160, v122, v123, v160
	v_min3_i32 v160, v124, v125, v160
	v_min3_i32 v160, v126, v127, v160
	v_min3_i32 v160, v128, v129, v160
	v_min3_i32 v160, v130, v131, v160
	v_min3_i32 v160, v132, v133, v160
	v_min3_i32 v157, v134, v135, v160
	v_mfma_f32_16x16x32_f16 v[120:123], v[48:51], v[112:115], 0
	v_mfma_f32_16x16x32_f16 v[124:127], v[52:55], v[112:115], 0
	v_mov_b32_e32 v158, 0
	v_mfma_f32_16x16x32_f16 v[128:131], v[56:59], v[112:115], 0
	v_mfma_f32_16x16x32_f16 v[132:135], v[60:63], v[112:115], 0
	v_min3_i32 v160, v136, v137, v157
	v_min3_i32 v160, v138, v139, v160
	v_min3_i32 v160, v140, v141, v160
	v_min3_i32 v160, v142, v143, v160
	v_min3_i32 v160, v144, v145, v160
	v_min3_i32 v160, v146, v147, v160
	v_min3_i32 v160, v148, v149, v160
	v_min3_i32 v156, v150, v151, v160
	v_cmp_ge_i32_e32 vcc, v156, v157
	v_mfma_f32_16x16x32_f16 v[136:139], v[64:67], v[112:115], 0
	v_mfma_f32_16x16x32_f16 v[140:143], v[68:71], v[112:115], 0
	v_cndmask_b32_e32 v158, 1, v158, vcc
	v_mfma_f32_16x16x32_f16 v[144:147], v[72:75], v[112:115], 0
	v_mfma_f32_16x16x32_f16 v[148:151], v[76:79], v[112:115], 0
	v_min3_i32 v160, v120, v121, v156
	v_min3_i32 v160, v122, v123, v160
	v_min3_i32 v160, v124, v125, v160
	v_min3_i32 v160, v126, v127, v160
	v_min3_i32 v160, v128, v129, v160
	v_min3_i32 v160, v130, v131, v160
	v_min3_i32 v160, v132, v133, v160
	v_min3_i32 v157, v134, v135, v160
	v_cmp_ge_i32_e32 vcc, v157, v156
	v_mfma_f32_16x16x32_f16 v[120:123], v[80:83], v[112:115], 0
	v_mfma_f32_16x16x32_f16 v[124:127], v[84:87], v[112:115], 0
	v_cndmask_b32_e32 v158, 2, v158, vcc
	v_mfma_f32_16x16x32_f16 v[128:131], v[88:91], v[112:115], 0
	v_mfma_f32_16x16x32_f16 v[132:135], v[92:95], v[112:115], 0
	v_min3_i32 v160, v136, v137, v157
	v_min3_i32 v160, v138, v139, v160
	v_min3_i32 v160, v140, v141, v160
	v_min3_i32 v160, v142, v143, v160
	v_min3_i32 v160, v144, v145, v160
	v_min3_i32 v160, v146, v147, v160
	v_min3_i32 v160, v148, v149, v160
	v_min3_i32 v156, v150, v151, v160
	v_cmp_ge_i32_e32 vcc, v156, v157
	v_mfma_f32_16x16x32_f16 v[136:139], v[96:99], v[112:115], 0
	v_mfma_f32_16x16x32_f16 v[140:143], v[100:103], v[112:115], 0
	v_cndmask_b32_e32 v158, 3, v158, vcc
	v_mfma_f32_16x16x32_f16 v[144:147], v[104:107], v[112:115], 0
	v_mfma_f32_16x16x32_f16 v[148:151], v[108:111], v[112:115], 0
	v_min3_i32 v160, v120, v121, v156
	v_min3_i32 v160, v122, v123, v160
	v_min3_i32 v160, v124, v125, v160
	v_min3_i32 v160, v126, v127, v160
	v_min3_i32 v160, v128, v129, v160
	v_min3_i32 v160, v130, v131, v160
	v_min3_i32 v160, v132, v133, v160
	v_min3_i32 v157, v134, v135, v160
	v_cmp_ge_i32_e32 vcc, v157, v156
	s_waitcnt vmcnt(0)
	global_load_dwordx4 v[112:115], v164, s[22:23]
	v_mfma_f32_16x16x32_f16 v[120:123], v[16:19], v[116:119], 0
	v_mfma_f32_16x16x32_f16 v[124:127], v[20:23], v[116:119], 0
	v_cndmask_b32_e32 v158, 4, v158, vcc
	v_mfma_f32_16x16x32_f16 v[128:131], v[24:27], v[116:119], 0
	v_mfma_f32_16x16x32_f16 v[132:135], v[28:31], v[116:119], 0
	v_min3_i32 v160, v136, v137, v157
	v_min3_i32 v160, v138, v139, v160
	v_min3_i32 v160, v140, v141, v160
	v_min3_i32 v160, v142, v143, v160
	v_min3_i32 v160, v144, v145, v160
	v_min3_i32 v160, v146, v147, v160
	v_min3_i32 v160, v148, v149, v160
	v_min3_i32 v156, v150, v151, v160
	v_cmp_ge_i32_e32 vcc, v156, v157
	v_mfma_f32_16x16x32_f16 v[136:139], v[32:35], v[116:119], 0
	v_mfma_f32_16x16x32_f16 v[140:143], v[36:39], v[116:119], 0
	v_cndmask_b32_e32 v158, 5, v158, vcc
	v_add_u32_e32 v162, s40, v158
	v_lshl_or_b32 v162, v162, 2, v166
	v_mov_b32_e32 v163, v156
	ds_min_u64 v167, v[162:163] offset:16640
	v_mfma_f32_16x16x32_f16 v[144:147], v[40:43], v[116:119], 0
	v_mfma_f32_16x16x32_f16 v[148:151], v[44:47], v[116:119], 0
	v_min3_i32 v160, v120, v121, s41
	v_min3_i32 v160, v122, v123, v160
	v_min3_i32 v160, v124, v125, v160
	v_min3_i32 v160, v126, v127, v160
	v_min3_i32 v160, v128, v129, v160
	v_min3_i32 v160, v130, v131, v160
	v_min3_i32 v160, v132, v133, v160
	v_min3_i32 v157, v134, v135, v160
	s_waitcnt lgkmcnt(0)
	s_barrier
	s_cmp_lt_u32 s50, 3
	s_cbranch_scc0 .Lp1a_3_x
	s_lshl_b32 s60, s50, 7
	v_add_u32_e32 v2, s60, v169
	ds_read_b32 v178, v2 offset:16384
	s_lshl_b32 s60, s50, 4
	v_add_u32_e32 v2, s60, v177
	v_mul_u32_u24_e32 v3, 0x556, v2
	v_lshrrev_b32_e32 v3, 16, v3
	v_mul_u32_u24_e32 v4, 48, v3
	v_sub_u32_e32 v4, v2, v4
	v_mul_u32_u24_e32 v3, 0x6c0, v3
	v_mad_u32_u24 v215, v4, 12, v3
	v_add_u32_e32 v215, v215, v175
	s_lshl_b32 s60, s50, 10
	v_add_u32_e32 v210, s60, v170
.Lp1a_3_x:
	v_mfma_f32_16x16x32_f16 v[120:123], v[48:51], v[116:119], 0
	v_mfma_f32_16x16x32_f16 v[124:127], v[52:55], v[116:119], 0
	v_mov_b32_e32 v158, 0
	v_mfma_f32_16x16x32_f16 v[128:131], v[56:59], v[116:119], 0
	v_mfma_f32_16x16x32_f16 v[132:135], v[60:63], v[116:119], 0
	v_min3_i32 v160, v136, v137, v157
	v_min3_i32 v160, v138, v139, v160
	v_min3_i32 v160, v140, v141, v160
	v_min3_i32 v160, v142, v143, v160
	v_min3_i32 v160, v144, v145, v160
	v_min3_i32 v160, v146, v147, v160
	v_min3_i32 v160, v148, v149, v160
	v_min3_i32 v156, v150, v151, v160
	v_cmp_ge_i32_e32 vcc, v156, v157
	s_waitcnt lgkmcnt(0)
	s_cmp_lt_u32 s50, 3
	s_cbranch_scc0 .Lp1b_3_x
	v_lshrrev_b32_e32 v2, 2, v178
	v_mul_u32_u24_e32 v3, 43, v2
	v_lshrrev_b32_e32 v3, 8, v3
	v_mul_u32_u24_e32 v4, 6, v3
	v_sub_u32_e32 v4, v2, v4
	v_mul_u32_u24_e32 v3, 24, v3
	v_min_u32_e32 v3, 0xa5, v3
	v_lshl_add_u32 v3, v4, 2, v3
	v_lshrrev_b32_e32 v4, 2, v168
	v_add_u32_e32 v3, v3, v4
	v_and_b32_e32 v4, 3, v178
	v_lshlrev_b32_e32 v4, 2, v4
	v_and_b32_e32 v5, 3, v168
	v_or_b32_e32 v4, v4, v5
	v_lshl_or_b32 v214, v3, 4, v4
	v_add_u32_e32 v3, s9, v3
	v_lshlrev_b32_e32 v4, 4, v4
	v_lshl_or_b32 v206, v3, 10, v4
	global_load_dwordx4 v[178:181], v206, s[6:7]
	global_load_dwordx4 v[182:185], v206, s[6:7] offset:256
	global_load_dwordx4 v[186:189], v206, s[6:7] offset:512
	global_load_dwordx4 v[190:193], v206, s[6:7] offset:768
	global_load_dwordx4 v[194:197], v206, s[6:7] offset:2048
	global_load_dwordx4 v[198:201], v206, s[6:7] offset:2304
	global_load_dwordx4 v[202:205], v206, s[6:7] offset:2560
	global_load_dwordx4 v[206:209], v206, s[6:7] offset:2816
	global_load_dwordx4 v[210:213], v210, s[4:5]
.Lp1b_3_x:
	v_mfma_f32_16x16x32_f16 v[136:139], v[64:67], v[116:119], 0
	v_mfma_f32_16x16x32_f16 v[140:143], v[68:71], v[116:119], 0
	v_cndmask_b32_e32 v158, 1, v158, vcc
	v_mfma_f32_16x16x32_f16 v[144:147], v[72:75], v[116:119], 0
	v_mfma_f32_16x16x32_f16 v[148:151], v[76:79], v[116:119], 0
	v_min3_i32 v160, v120, v121, v156
	v_min3_i32 v160, v122, v123, v160
	v_min3_i32 v160, v124, v125, v160
	v_min3_i32 v160, v126, v127, v160
	v_min3_i32 v160, v128, v129, v160
	v_min3_i32 v160, v130, v131, v160
	v_min3_i32 v160, v132, v133, v160
	v_min3_i32 v157, v134, v135, v160
	v_cmp_ge_i32_e32 vcc, v157, v156
	v_mfma_f32_16x16x32_f16 v[120:123], v[80:83], v[116:119], 0
	v_mfma_f32_16x16x32_f16 v[124:127], v[84:87], v[116:119], 0
	v_cndmask_b32_e32 v158, 2, v158, vcc
	v_mfma_f32_16x16x32_f16 v[128:131], v[88:91], v[116:119], 0
	v_mfma_f32_16x16x32_f16 v[132:135], v[92:95], v[116:119], 0
	v_min3_i32 v160, v136, v137, v157
	v_min3_i32 v160, v138, v139, v160
	v_min3_i32 v160, v140, v141, v160
	v_min3_i32 v160, v142, v143, v160
	v_min3_i32 v160, v144, v145, v160
	v_min3_i32 v160, v146, v147, v160
	v_min3_i32 v160, v148, v149, v160
	v_min3_i32 v156, v150, v151, v160
	v_cmp_ge_i32_e32 vcc, v156, v157
	v_mfma_f32_16x16x32_f16 v[136:139], v[96:99], v[116:119], 0
	v_mfma_f32_16x16x32_f16 v[140:143], v[100:103], v[116:119], 0
	v_cndmask_b32_e32 v158, 3, v158, vcc
	v_mfma_f32_16x16x32_f16 v[144:147], v[104:107], v[116:119], 0
	v_mfma_f32_16x16x32_f16 v[148:151], v[108:111], v[116:119], 0
	v_min3_i32 v160, v120, v121, v156
	v_min3_i32 v160, v122, v123, v160
	v_min3_i32 v160, v124, v125, v160
	v_min3_i32 v160, v126, v127, v160
	v_min3_i32 v160, v128, v129, v160
	v_min3_i32 v160, v130, v131, v160
	v_min3_i32 v160, v132, v133, v160
	v_min3_i32 v157, v134, v135, v160
	v_cmp_ge_i32_e32 vcc, v157, v156
	s_waitcnt vmcnt(0)
	global_load_dwordx4 v[116:119], v164, s[22:23] offset:1024
	v_mfma_f32_16x16x32_f16 v[120:123], v[16:19], v[112:115], 0
	v_mfma_f32_16x16x32_f16 v[124:127], v[20:23], v[112:115], 0
	v_cndmask_b32_e32 v158, 4, v158, vcc
	v_mfma_f32_16x16x32_f16 v[128:131], v[24:27], v[112:115], 0
	v_mfma_f32_16x16x32_f16 v[132:135], v[28:31], v[112:115], 0
	v_min3_i32 v160, v136, v137, v157
	v_min3_i32 v160, v138, v139, v160
	v_min3_i32 v160, v140, v141, v160
	v_min3_i32 v160, v142, v143, v160
	v_min3_i32 v160, v144, v145, v160
	v_min3_i32 v160, v146, v147, v160
	v_min3_i32 v160, v148, v149, v160
	v_min3_i32 v156, v150, v151, v160
	v_cmp_ge_i32_e32 vcc, v156, v157
	v_mfma_f32_16x16x32_f16 v[136:139], v[32:35], v[112:115], 0
	v_mfma_f32_16x16x32_f16 v[140:143], v[36:39], v[112:115], 0
	v_cndmask_b32_e32 v158, 5, v158, vcc
	v_add_u32_e32 v162, s40, v158
	v_lshl_or_b32 v162, v162, 2, v166
	v_mov_b32_e32 v163, v156
	ds_min_u64 v167, v[162:163] offset:16768
	v_mfma_f32_16x16x32_f16 v[144:147], v[40:43], v[112:115], 0
	v_mfma_f32_16x16x32_f16 v[148:151], v[44:47], v[112:115], 0
	v_min3_i32 v160, v120, v121, s41
	v_min3_i32 v160, v122, v123, v160
	v_min3_i32 v160, v124, v125, v160
	v_min3_i32 v160, v126, v127, v160
	v_min3_i32 v160, v128, v129, v160
	v_min3_i32 v160, v130, v131, v160
	v_min3_i32 v160, v132, v133, v160
	v_min3_i32 v157, v134, v135, v160
	v_mfma_f32_16x16x32_f16 v[120:123], v[48:51], v[112:115], 0
	v_mfma_f32_16x16x32_f16 v[124:127], v[52:55], v[112:115], 0
	v_mov_b32_e32 v158, 0
	v_mfma_f32_16x16x32_f16 v[128:131], v[56:59], v[112:115], 0
	v_mfma_f32_16x16x32_f16 v[132:135], v[60:63], v[112:115], 0
	v_min3_i32 v160, v136, v137, v157
	v_min3_i32 v160, v138, v139, v160
	v_min3_i32 v160, v140, v141, v160
	v_min3_i32 v160, v142, v143, v160
	v_min3_i32 v160, v144, v145, v160
	v_min3_i32 v160, v146, v147, v160
	v_min3_i32 v160, v148, v149, v160
	v_min3_i32 v156, v150, v151, v160
	v_cmp_ge_i32_e32 vcc, v156, v157
	v_mfma_f32_16x16x32_f16 v[136:139], v[64:67], v[112:115], 0
	v_mfma_f32_16x16x32_f16 v[140:143], v[68:71], v[112:115], 0
	v_cndmask_b32_e32 v158, 1, v158, vcc
	v_mfma_f32_16x16x32_f16 v[144:147], v[72:75], v[112:115], 0
	v_mfma_f32_16x16x32_f16 v[148:151], v[76:79], v[112:115], 0
	v_min3_i32 v160, v120, v121, v156
	v_min3_i32 v160, v122, v123, v160
	v_min3_i32 v160, v124, v125, v160
	v_min3_i32 v160, v126, v127, v160
	v_min3_i32 v160, v128, v129, v160
	v_min3_i32 v160, v130, v131, v160
	v_min3_i32 v160, v132, v133, v160
	v_min3_i32 v157, v134, v135, v160
	v_cmp_ge_i32_e32 vcc, v157, v156
	v_mfma_f32_16x16x32_f16 v[120:123], v[80:83], v[112:115], 0
	v_mfma_f32_16x16x32_f16 v[124:127], v[84:87], v[112:115], 0
	v_cndmask_b32_e32 v158, 2, v158, vcc
	v_mfma_f32_16x16x32_f16 v[128:131], v[88:91], v[112:115], 0
	v_mfma_f32_16x16x32_f16 v[132:135], v[92:95], v[112:115], 0
	v_min3_i32 v160, v136, v137, v157
	v_min3_i32 v160, v138, v139, v160
	v_min3_i32 v160, v140, v141, v160
	v_min3_i32 v160, v142, v143, v160
	v_min3_i32 v160, v144, v145, v160
	v_min3_i32 v160, v146, v147, v160
	v_min3_i32 v160, v148, v149, v160
	v_min3_i32 v156, v150, v151, v160
	v_cmp_ge_i32_e32 vcc, v156, v157
	v_mfma_f32_16x16x32_f16 v[136:139], v[96:99], v[112:115], 0
	v_mfma_f32_16x16x32_f16 v[140:143], v[100:103], v[112:115], 0
	v_cndmask_b32_e32 v158, 3, v158, vcc
	v_mfma_f32_16x16x32_f16 v[144:147], v[104:107], v[112:115], 0
	v_mfma_f32_16x16x32_f16 v[148:151], v[108:111], v[112:115], 0
	v_min3_i32 v160, v120, v121, v156
	v_min3_i32 v160, v122, v123, v160
	v_min3_i32 v160, v124, v125, v160
	v_min3_i32 v160, v126, v127, v160
	v_min3_i32 v160, v128, v129, v160
	v_min3_i32 v160, v130, v131, v160
	v_min3_i32 v160, v132, v133, v160
	v_min3_i32 v157, v134, v135, v160
	v_cmp_ge_i32_e32 vcc, v157, v156
	s_waitcnt vmcnt(0)
	global_load_dwordx4 v[112:115], v164, s[22:23] offset:2048
	v_mfma_f32_16x16x32_f16 v[120:123], v[16:19], v[116:119], 0
	v_mfma_f32_16x16x32_f16 v[124:127], v[20:23], v[116:119], 0
	v_cndmask_b32_e32 v158, 4, v158, vcc
	v_mfma_f32_16x16x32_f16 v[128:131], v[24:27], v[116:119], 0
	v_mfma_f32_16x16x32_f16 v[132:135], v[28:31], v[116:119], 0
	v_min3_i32 v160, v136, v137, v157
	v_min3_i32 v160, v138, v139, v160
	v_min3_i32 v160, v140, v141, v160
	v_min3_i32 v160, v142, v143, v160
	v_min3_i32 v160, v144, v145, v160
	v_min3_i32 v160, v146, v147, v160
	v_min3_i32 v160, v148, v149, v160
	v_min3_i32 v156, v150, v151, v160
	v_cmp_ge_i32_e32 vcc, v156, v157
	v_mfma_f32_16x16x32_f16 v[136:139], v[32:35], v[116:119], 0
	v_mfma_f32_16x16x32_f16 v[140:143], v[36:39], v[116:119], 0
	v_cndmask_b32_e32 v158, 5, v158, vcc
	v_add_u32_e32 v162, s40, v158
	v_lshl_or_b32 v162, v162, 2, v166
	v_mov_b32_e32 v163, v156
	ds_min_u64 v167, v[162:163] offset:16896
	v_mfma_f32_16x16x32_f16 v[144:147], v[40:43], v[116:119], 0
	v_mfma_f32_16x16x32_f16 v[148:151], v[44:47], v[116:119], 0
	v_min3_i32 v160, v120, v121, s41
	v_min3_i32 v160, v122, v123, v160
	v_min3_i32 v160, v124, v125, v160
	v_min3_i32 v160, v126, v127, v160
	v_min3_i32 v160, v128, v129, v160
	v_min3_i32 v160, v130, v131, v160
	v_min3_i32 v160, v132, v133, v160
	v_min3_i32 v157, v134, v135, v160
	v_mfma_f32_16x16x32_f16 v[120:123], v[48:51], v[116:119], 0
	v_mfma_f32_16x16x32_f16 v[124:127], v[52:55], v[116:119], 0
	v_mov_b32_e32 v158, 0
	v_mfma_f32_16x16x32_f16 v[128:131], v[56:59], v[116:119], 0
	v_mfma_f32_16x16x32_f16 v[132:135], v[60:63], v[116:119], 0
	v_min3_i32 v160, v136, v137, v157
	v_min3_i32 v160, v138, v139, v160
	v_min3_i32 v160, v140, v141, v160
	v_min3_i32 v160, v142, v143, v160
	v_min3_i32 v160, v144, v145, v160
	v_min3_i32 v160, v146, v147, v160
	v_min3_i32 v160, v148, v149, v160
	v_min3_i32 v156, v150, v151, v160
	v_cmp_ge_i32_e32 vcc, v156, v157
	v_mfma_f32_16x16x32_f16 v[136:139], v[64:67], v[116:119], 0
	v_mfma_f32_16x16x32_f16 v[140:143], v[68:71], v[116:119], 0
	v_cndmask_b32_e32 v158, 1, v158, vcc
	v_mfma_f32_16x16x32_f16 v[144:147], v[72:75], v[116:119], 0
	v_mfma_f32_16x16x32_f16 v[148:151], v[76:79], v[116:119], 0
	v_min3_i32 v160, v120, v121, v156
	v_min3_i32 v160, v122, v123, v160
	v_min3_i32 v160, v124, v125, v160
	v_min3_i32 v160, v126, v127, v160
	v_min3_i32 v160, v128, v129, v160
	v_min3_i32 v160, v130, v131, v160
	v_min3_i32 v160, v132, v133, v160
	v_min3_i32 v157, v134, v135, v160
	v_cmp_ge_i32_e32 vcc, v157, v156
	v_mfma_f32_16x16x32_f16 v[120:123], v[80:83], v[116:119], 0
	v_mfma_f32_16x16x32_f16 v[124:127], v[84:87], v[116:119], 0
	v_cndmask_b32_e32 v158, 2, v158, vcc
	v_mfma_f32_16x16x32_f16 v[128:131], v[88:91], v[116:119], 0
	v_mfma_f32_16x16x32_f16 v[132:135], v[92:95], v[116:119], 0
	v_min3_i32 v160, v136, v137, v157
	v_min3_i32 v160, v138, v139, v160
	v_min3_i32 v160, v140, v141, v160
	v_min3_i32 v160, v142, v143, v160
	v_min3_i32 v160, v144, v145, v160
	v_min3_i32 v160, v146, v147, v160
	v_min3_i32 v160, v148, v149, v160
	v_min3_i32 v156, v150, v151, v160
	v_cmp_ge_i32_e32 vcc, v156, v157
	v_mfma_f32_16x16x32_f16 v[136:139], v[96:99], v[116:119], 0
	v_mfma_f32_16x16x32_f16 v[140:143], v[100:103], v[116:119], 0
	v_cndmask_b32_e32 v158, 3, v158, vcc
	v_mfma_f32_16x16x32_f16 v[144:147], v[104:107], v[116:119], 0
	v_mfma_f32_16x16x32_f16 v[148:151], v[108:111], v[116:119], 0
	v_min3_i32 v160, v120, v121, v156
	v_min3_i32 v160, v122, v123, v160
	v_min3_i32 v160, v124, v125, v160
	v_min3_i32 v160, v126, v127, v160
	v_min3_i32 v160, v128, v129, v160
	v_min3_i32 v160, v130, v131, v160
	v_min3_i32 v160, v132, v133, v160
	v_min3_i32 v157, v134, v135, v160
	v_cmp_ge_i32_e32 vcc, v157, v156
	s_waitcnt vmcnt(0)
	global_load_dwordx4 v[116:119], v164, s[22:23] offset:3072
	v_mfma_f32_16x16x32_f16 v[120:123], v[16:19], v[112:115], 0
	v_mfma_f32_16x16x32_f16 v[124:127], v[20:23], v[112:115], 0
	v_cndmask_b32_e32 v158, 4, v158, vcc
	v_mfma_f32_16x16x32_f16 v[128:131], v[24:27], v[112:115], 0
	v_mfma_f32_16x16x32_f16 v[132:135], v[28:31], v[112:115], 0
	v_min3_i32 v160, v136, v137, v157
	v_min3_i32 v160, v138, v139, v160
	v_min3_i32 v160, v140, v141, v160
	v_min3_i32 v160, v142, v143, v160
	v_min3_i32 v160, v144, v145, v160
	v_min3_i32 v160, v146, v147, v160
	v_min3_i32 v160, v148, v149, v160
	v_min3_i32 v156, v150, v151, v160
	v_cmp_ge_i32_e32 vcc, v156, v157
	v_mfma_f32_16x16x32_f16 v[136:139], v[32:35], v[112:115], 0
	v_mfma_f32_16x16x32_f16 v[140:143], v[36:39], v[112:115], 0
	v_cndmask_b32_e32 v158, 5, v158, vcc
	v_add_u32_e32 v162, s40, v158
	v_lshl_or_b32 v162, v162, 2, v166
	v_mov_b32_e32 v163, v156
	ds_min_u64 v167, v[162:163] offset:17024
	v_mfma_f32_16x16x32_f16 v[144:147], v[40:43], v[112:115], 0
	v_mfma_f32_16x16x32_f16 v[148:151], v[44:47], v[112:115], 0
	v_min3_i32 v160, v120, v121, s41
	v_min3_i32 v160, v122, v123, v160
	v_min3_i32 v160, v124, v125, v160
	v_min3_i32 v160, v126, v127, v160
	v_min3_i32 v160, v128, v129, v160
	v_min3_i32 v160, v130, v131, v160
	v_min3_i32 v160, v132, v133, v160
	v_min3_i32 v157, v134, v135, v160
	s_waitcnt lgkmcnt(0)
	s_barrier
	s_cmp_eq_u32 s50, 3
	s_cbranch_scc0 .Lp1a_6_x
	s_lshl_b32 s60, s50, 7
	v_add_u32_e32 v2, s60, v169
	ds_read_b32 v178, v2 offset:16384
	s_lshl_b32 s60, s50, 4
	v_add_u32_e32 v2, s60, v177
	v_mul_u32_u24_e32 v3, 0x556, v2
	v_lshrrev_b32_e32 v3, 16, v3
	v_mul_u32_u24_e32 v4, 48, v3
	v_sub_u32_e32 v4, v2, v4
	v_mul_u32_u24_e32 v3, 0x6c0, v3
	v_mad_u32_u24 v215, v4, 12, v3
	v_add_u32_e32 v215, v215, v175
	s_lshl_b32 s60, s50, 10
	v_add_u32_e32 v210, s60, v170
.Lp1a_6_x:
	s_cmp_lt_u32 s50, 2
	s_cbranch_scc0 .Lp1a_6_y
	s_add_i32 s65, s50, 4
	s_lshl_b32 s60, s65, 7
	v_add_u32_e32 v2, s60, v169
	ds_read_b32 v216, v2 offset:16384
	s_lshl_b32 s60, s65, 4
	v_add_u32_e32 v2, s60, v177
	v_mul_u32_u24_e32 v3, 0x556, v2
	v_lshrrev_b32_e32 v3, 16, v3
	v_mul_u32_u24_e32 v4, 48, v3
	v_sub_u32_e32 v4, v2, v4
	v_mul_u32_u24_e32 v3, 0x6c0, v3
	v_mad_u32_u24 v253, v4, 12, v3
	v_add_u32_e32 v253, v253, v175
	s_lshl_b32 s60, s65, 10
	v_add_u32_e32 v248, s60, v170
.Lp1a_6_y:
	v_mfma_f32_16x16x32_f16 v[120:123], v[48:51], v[112:115], 0
	v_mfma_f32_16x16x32_f16 v[124:127], v[52:55], v[112:115], 0
	v_mov_b32_e32 v158, 0
	v_mfma_f32_16x16x32_f16 v[128:131], v[56:59], v[112:115], 0
	v_mfma_f32_16x16x32_f16 v[132:135], v[60:63], v[112:115], 0
	v_min3_i32 v160, v136, v137, v157
	v_min3_i32 v160, v138, v139, v160
	v_min3_i32 v160, v140, v141, v160
	v_min3_i32 v160, v142, v143, v160
	v_min3_i32 v160, v144, v145, v160
	v_min3_i32 v160, v146, v147, v160
	v_min3_i32 v160, v148, v149, v160
	v_min3_i32 v156, v150, v151, v160
	v_cmp_ge_i32_e32 vcc, v156, v157
	s_waitcnt lgkmcnt(0)
	s_cmp_eq_u32 s50, 3
	s_cbranch_scc0 .Lp1b_6_x
	v_lshrrev_b32_e32 v2, 2, v178
	v_mul_u32_u24_e32 v3, 43, v2
	v_lshrrev_b32_e32 v3, 8, v3
	v_mul_u32_u24_e32 v4, 6, v3
	v_sub_u32_e32 v4, v2, v4
	v_mul_u32_u24_e32 v3, 24, v3
	v_min_u32_e32 v3, 0xa5, v3
	v_lshl_add_u32 v3, v4, 2, v3
	v_lshrrev_b32_e32 v4, 2, v168
	v_add_u32_e32 v3, v3, v4
	v_and_b32_e32 v4, 3, v178
	v_lshlrev_b32_e32 v4, 2, v4
	v_and_b32_e32 v5, 3, v168
	v_or_b32_e32 v4, v4, v5
	v_lshl_or_b32 v214, v3, 4, v4
	v_add_u32_e32 v3, s9, v3
	v_lshlrev_b32_e32 v4, 4, v4
	v_lshl_or_b32 v206, v3, 10, v4
	global_load_dwordx4 v[178:181], v206, s[6:7]
	global_load_dwordx4 v[182:185], v206, s[6:7] offset:256
	global_load_dwordx4 v[186:189], v206, s[6:7] offset:512
	global_load_dwordx4 v[190:193], v206, s[6:7] offset:768
	global_load_dwordx4 v[194:197], v206, s[6:7] offset:2048
	global_load_dwordx4 v[198:201], v206, s[6:7] offset:2304
	global_load_dwordx4 v[202:205], v206, s[6:7] offset:2560
	global_load_dwordx4 v[206:209], v206, s[6:7] offset:2816
	global_load_dwordx4 v[210:213], v210, s[4:5]
.Lp1b_6_x:
	s_cmp_lt_u32 s50, 2
	s_cbranch_scc0 .Lp1b_6_y
	v_lshrrev_b32_e32 v2, 2, v216
	v_mul_u32_u24_e32 v3, 43, v2
	v_lshrrev_b32_e32 v3, 8, v3
	v_mul_u32_u24_e32 v4, 6, v3
	v_sub_u32_e32 v4, v2, v4
	v_mul_u32_u24_e32 v3, 24, v3
	v_min_u32_e32 v3, 0xa5, v3
	v_lshl_add_u32 v3, v4, 2, v3
	v_lshrrev_b32_e32 v4, 2, v168
	v_add_u32_e32 v3, v3, v4
	v_and_b32_e32 v4, 3, v216
	v_lshlrev_b32_e32 v4, 2, v4
	v_and_b32_e32 v5, 3, v168
	v_or_b32_e32 v4, v4, v5
	v_lshl_or_b32 v252, v3, 4, v4
	v_add_u32_e32 v3, s9, v3
	v_lshlrev_b32_e32 v4, 4, v4
	v_lshl_or_b32 v244, v3, 10, v4
	global_load_dwordx4 v[216:219], v244, s[6:7]
	global_load_dwordx4 v[220:223], v244, s[6:7] offset:256
	global_load_dwordx4 v[224:227], v244, s[6:7] offset:512
	global_load_dwordx4 v[228:231], v244, s[6:7] offset:768
	global_load_dwordx4 v[232:235], v244, s[6:7] offset:2048
	global_load_dwordx4 v[236:239], v244, s[6:7] offset:2304
	global_load_dwordx4 v[240:243], v244, s[6:7] offset:2560
	global_load_dwordx4 v[244:247], v244, s[6:7] offset:2816
	global_load_dwordx4 v[248:251], v248, s[4:5]
.Lp1b_6_y:
	v_mfma_f32_16x16x32_f16 v[136:139], v[64:67], v[112:115], 0
	v_mfma_f32_16x16x32_f16 v[140:143], v[68:71], v[112:115], 0
	v_cndmask_b32_e32 v158, 1, v158, vcc
	v_mfma_f32_16x16x32_f16 v[144:147], v[72:75], v[112:115], 0
	v_mfma_f32_16x16x32_f16 v[148:151], v[76:79], v[112:115], 0
	v_min3_i32 v160, v120, v121, v156
	v_min3_i32 v160, v122, v123, v160
	v_min3_i32 v160, v124, v125, v160
	v_min3_i32 v160, v126, v127, v160
	v_min3_i32 v160, v128, v129, v160
	v_min3_i32 v160, v130, v131, v160
	v_min3_i32 v160, v132, v133, v160
	v_min3_i32 v157, v134, v135, v160
	v_cmp_ge_i32_e32 vcc, v157, v156
	v_mfma_f32_16x16x32_f16 v[120:123], v[80:83], v[112:115], 0
	v_mfma_f32_16x16x32_f16 v[124:127], v[84:87], v[112:115], 0
	v_cndmask_b32_e32 v158, 2, v158, vcc
	v_mfma_f32_16x16x32_f16 v[128:131], v[88:91], v[112:115], 0
	v_mfma_f32_16x16x32_f16 v[132:135], v[92:95], v[112:115], 0
	v_min3_i32 v160, v136, v137, v157
	v_min3_i32 v160, v138, v139, v160
	v_min3_i32 v160, v140, v141, v160
	v_min3_i32 v160, v142, v143, v160
	v_min3_i32 v160, v144, v145, v160
	v_min3_i32 v160, v146, v147, v160
	v_min3_i32 v160, v148, v149, v160
	v_min3_i32 v156, v150, v151, v160
	v_cmp_ge_i32_e32 vcc, v156, v157
	v_mfma_f32_16x16x32_f16 v[136:139], v[96:99], v[112:115], 0
	v_mfma_f32_16x16x32_f16 v[140:143], v[100:103], v[112:115], 0
	v_cndmask_b32_e32 v158, 3, v158, vcc
	v_mfma_f32_16x16x32_f16 v[144:147], v[104:107], v[112:115], 0
	v_mfma_f32_16x16x32_f16 v[148:151], v[108:111], v[112:115], 0
	v_min3_i32 v160, v120, v121, v156
	v_min3_i32 v160, v122, v123, v160
	v_min3_i32 v160, v124, v125, v160
	v_min3_i32 v160, v126, v127, v160
	v_min3_i32 v160, v128, v129, v160
	v_min3_i32 v160, v130, v131, v160
	v_min3_i32 v160, v132, v133, v160
	v_min3_i32 v157, v134, v135, v160
	v_cmp_ge_i32_e32 vcc, v157, v156
	s_waitcnt vmcnt(0)
	global_load_dwordx4 v[112:115], v164, s[24:25]
	v_mfma_f32_16x16x32_f16 v[120:123], v[16:19], v[116:119], 0
	v_mfma_f32_16x16x32_f16 v[124:127], v[20:23], v[116:119], 0
	v_cndmask_b32_e32 v158, 4, v158, vcc
	v_mfma_f32_16x16x32_f16 v[128:131], v[24:27], v[116:119], 0
	v_mfma_f32_16x16x32_f16 v[132:135], v[28:31], v[116:119], 0
	v_min3_i32 v160, v136, v137, v157
	v_min3_i32 v160, v138, v139, v160
	v_min3_i32 v160, v140, v141, v160
	v_min3_i32 v160, v142, v143, v160
	v_min3_i32 v160, v144, v145, v160
	v_min3_i32 v160, v146, v147, v160
	v_min3_i32 v160, v148, v149, v160
	v_min3_i32 v156, v150, v151, v160
	v_cmp_ge_i32_e32 vcc, v156, v157
	v_mfma_f32_16x16x32_f16 v[136:139], v[32:35], v[116:119], 0
	v_mfma_f32_16x16x32_f16 v[140:143], v[36:39], v[116:119], 0
	v_cndmask_b32_e32 v158, 5, v158, vcc
	v_add_u32_e32 v162, s40, v158
	v_lshl_or_b32 v162, v162, 2, v166
	v_mov_b32_e32 v163, v156
	ds_min_u64 v167, v[162:163] offset:17152
	v_mfma_f32_16x16x32_f16 v[144:147], v[40:43], v[116:119], 0
	v_mfma_f32_16x16x32_f16 v[148:151], v[44:47], v[116:119], 0
	v_min3_i32 v160, v120, v121, s41
	v_min3_i32 v160, v122, v123, v160
	v_min3_i32 v160, v124, v125, v160
	v_min3_i32 v160, v126, v127, v160
	v_min3_i32 v160, v128, v129, v160
	v_min3_i32 v160, v130, v131, v160
	v_min3_i32 v160, v132, v133, v160
	v_min3_i32 v157, v134, v135, v160
	v_mfma_f32_16x16x32_f16 v[120:123], v[48:51], v[116:119], 0
	v_mfma_f32_16x16x32_f16 v[124:127], v[52:55], v[116:119], 0
	v_mov_b32_e32 v158, 0
	v_mfma_f32_16x16x32_f16 v[128:131], v[56:59], v[116:119], 0
	v_mfma_f32_16x16x32_f16 v[132:135], v[60:63], v[116:119], 0
	v_min3_i32 v160, v136, v137, v157
	v_min3_i32 v160, v138, v139, v160
	v_min3_i32 v160, v140, v141, v160
	v_min3_i32 v160, v142, v143, v160
	v_min3_i32 v160, v144, v145, v160
	v_min3_i32 v160, v146, v147, v160
	v_min3_i32 v160, v148, v149, v160
	v_min3_i32 v156, v150, v151, v160
	v_cmp_ge_i32_e32 vcc, v156, v157
	v_mfma_f32_16x16x32_f16 v[136:139], v[64:67], v[116:119], 0
	v_mfma_f32_16x16x32_f16 v[140:143], v[68:71], v[116:119], 0
	v_cndmask_b32_e32 v158, 1, v158, vcc
	v_mfma_f32_16x16x32_f16 v[144:147], v[72:75], v[116:119], 0
	v_mfma_f32_16x16x32_f16 v[148:151], v[76:79], v[116:119], 0
	v_min3_i32 v160, v120, v121, v156
	v_min3_i32 v160, v122, v123, v160
	v_min3_i32 v160, v124, v125, v160
	v_min3_i32 v160, v126, v127, v160
	v_min3_i32 v160, v128, v129, v160
	v_min3_i32 v160, v130, v131, v160
	v_min3_i32 v160, v132, v133, v160
	v_min3_i32 v157, v134, v135, v160
	v_cmp_ge_i32_e32 vcc, v157, v156
	v_mfma_f32_16x16x32_f16 v[120:123], v[80:83], v[116:119], 0
	v_mfma_f32_16x16x32_f16 v[124:127], v[84:87], v[116:119], 0
	v_cndmask_b32_e32 v158, 2, v158, vcc
	v_mfma_f32_16x16x32_f16 v[128:131], v[88:91], v[116:119], 0
	v_mfma_f32_16x16x32_f16 v[132:135], v[92:95], v[116:119], 0
	v_min3_i32 v160, v136, v137, v157
	v_min3_i32 v160, v138, v139, v160
	v_min3_i32 v160, v140, v141, v160
	v_min3_i32 v160, v142, v143, v160
	v_min3_i32 v160, v144, v145, v160
	v_min3_i32 v160, v146, v147, v160
	v_min3_i32 v160, v148, v149, v160
	v_min3_i32 v156, v150, v151, v160
	v_cmp_ge_i32_e32 vcc, v156, v157
	v_mfma_f32_16x16x32_f16 v[136:139], v[96:99], v[116:119], 0
	v_mfma_f32_16x16x32_f16 v[140:143], v[100:103], v[116:119], 0
	v_cndmask_b32_e32 v158, 3, v158, vcc
	v_mfma_f32_16x16x32_f16 v[144:147], v[104:107], v[116:119], 0
	v_mfma_f32_16x16x32_f16 v[148:151], v[108:111], v[116:119], 0
	v_min3_i32 v160, v120, v121, v156
	v_min3_i32 v160, v122, v123, v160
	v_min3_i32 v160, v124, v125, v160
	v_min3_i32 v160, v126, v127, v160
	v_min3_i32 v160, v128, v129, v160
	v_min3_i32 v160, v130, v131, v160
	v_min3_i32 v160, v132, v133, v160
	v_min3_i32 v157, v134, v135, v160
	v_cmp_ge_i32_e32 vcc, v157, v156
	s_waitcnt vmcnt(0)
	v_mfma_f32_16x16x32_f16 v[120:123], v[16:19], v[112:115], 0
	v_mfma_f32_16x16x32_f16 v[124:127], v[20:23], v[112:115], 0
	v_cndmask_b32_e32 v158, 4, v158, vcc
	v_mfma_f32_16x16x32_f16 v[128:131], v[24:27], v[112:115], 0
	v_mfma_f32_16x16x32_f16 v[132:135], v[28:31], v[112:115], 0
	v_min3_i32 v160, v136, v137, v157
	v_min3_i32 v160, v138, v139, v160
	v_min3_i32 v160, v140, v141, v160
	v_min3_i32 v160, v142, v143, v160
	v_min3_i32 v160, v144, v145, v160
	v_min3_i32 v160, v146, v147, v160
	v_min3_i32 v160, v148, v149, v160
	v_min3_i32 v156, v150, v151, v160
	v_cmp_ge_i32_e32 vcc, v156, v157
	v_mfma_f32_16x16x32_f16 v[136:139], v[32:35], v[112:115], 0
	v_mfma_f32_16x16x32_f16 v[140:143], v[36:39], v[112:115], 0
	v_cndmask_b32_e32 v158, 5, v158, vcc
	v_add_u32_e32 v162, s40, v158
	v_lshl_or_b32 v162, v162, 2, v166
	v_mov_b32_e32 v163, v156
	ds_min_u64 v167, v[162:163] offset:17280
	v_mfma_f32_16x16x32_f16 v[144:147], v[40:43], v[112:115], 0
	v_mfma_f32_16x16x32_f16 v[148:151], v[44:47], v[112:115], 0
	v_min3_i32 v160, v120, v121, s41
	v_min3_i32 v160, v122, v123, v160
	v_min3_i32 v160, v124, v125, v160
	v_min3_i32 v160, v126, v127, v160
	v_min3_i32 v160, v128, v129, v160
	v_min3_i32 v160, v130, v131, v160
	v_min3_i32 v160, v132, v133, v160
	v_min3_i32 v157, v134, v135, v160
	v_mfma_f32_16x16x32_f16 v[120:123], v[48:51], v[112:115], 0
	v_mfma_f32_16x16x32_f16 v[124:127], v[52:55], v[112:115], 0
	v_mov_b32_e32 v158, 0
	v_mfma_f32_16x16x32_f16 v[128:131], v[56:59], v[112:115], 0
	v_mfma_f32_16x16x32_f16 v[132:135], v[60:63], v[112:115], 0
	v_min3_i32 v160, v136, v137, v157
	v_min3_i32 v160, v138, v139, v160
	v_min3_i32 v160, v140, v141, v160
	v_min3_i32 v160, v142, v143, v160
	v_min3_i32 v160, v144, v145, v160
	v_min3_i32 v160, v146, v147, v160
	v_min3_i32 v160, v148, v149, v160
	v_min3_i32 v156, v150, v151, v160
	v_cmp_ge_i32_e32 vcc, v156, v157
	v_mfma_f32_16x16x32_f16 v[136:139], v[64:67], v[112:115], 0
	v_mfma_f32_16x16x32_f16 v[140:143], v[68:71], v[112:115], 0
	v_cndmask_b32_e32 v158, 1, v158, vcc
	v_mfma_f32_16x16x32_f16 v[144:147], v[72:75], v[112:115], 0
	v_mfma_f32_16x16x32_f16 v[148:151], v[76:79], v[112:115], 0
	v_min3_i32 v160, v120, v121, v156
	v_min3_i32 v160, v122, v123, v160
	v_min3_i32 v160, v124, v125, v160
	v_min3_i32 v160, v126, v127, v160
	v_min3_i32 v160, v128, v129, v160
	v_min3_i32 v160, v130, v131, v160
	v_min3_i32 v160, v132, v133, v160
	v_min3_i32 v157, v134, v135, v160
	v_cmp_ge_i32_e32 vcc, v157, v156
	v_mfma_f32_16x16x32_f16 v[120:123], v[80:83], v[112:115], 0
	v_mfma_f32_16x16x32_f16 v[124:127], v[84:87], v[112:115], 0
	v_cndmask_b32_e32 v158, 2, v158, vcc
	v_mfma_f32_16x16x32_f16 v[128:131], v[88:91], v[112:115], 0
	v_mfma_f32_16x16x32_f16 v[132:135], v[92:95], v[112:115], 0
	v_min3_i32 v160, v136, v137, v157
	v_min3_i32 v160, v138, v139, v160
	v_min3_i32 v160, v140, v141, v160
	v_min3_i32 v160, v142, v143, v160
	v_min3_i32 v160, v144, v145, v160
	v_min3_i32 v160, v146, v147, v160
	v_min3_i32 v160, v148, v149, v160
	v_min3_i32 v156, v150, v151, v160
	v_cmp_ge_i32_e32 vcc, v156, v157
	v_mfma_f32_16x16x32_f16 v[136:139], v[96:99], v[112:115], 0
	v_mfma_f32_16x16x32_f16 v[140:143], v[100:103], v[112:115], 0
	v_cndmask_b32_e32 v158, 3, v158, vcc
	v_mfma_f32_16x16x32_f16 v[144:147], v[104:107], v[112:115], 0
	v_mfma_f32_16x16x32_f16 v[148:151], v[108:111], v[112:115], 0
	v_min3_i32 v160, v120, v121, v156
	v_min3_i32 v160, v122, v123, v160
	v_min3_i32 v160, v124, v125, v160
	v_min3_i32 v160, v126, v127, v160
	v_min3_i32 v160, v128, v129, v160
	v_min3_i32 v160, v130, v131, v160
	v_min3_i32 v160, v132, v133, v160
	v_min3_i32 v157, v134, v135, v160
	v_cmp_ge_i32_e32 vcc, v157, v156
	s_nop 1
	v_cndmask_b32_e32 v158, 4, v158, vcc
	s_nop 7
	v_min3_i32 v160, v136, v137, v157
	v_min3_i32 v160, v138, v139, v160
	v_min3_i32 v160, v140, v141, v160
	v_min3_i32 v160, v142, v143, v160
	v_min3_i32 v160, v144, v145, v160
	v_min3_i32 v160, v146, v147, v160
	v_min3_i32 v160, v148, v149, v160
	v_min3_i32 v156, v150, v151, v160
	v_cmp_ge_i32_e32 vcc, v156, v157
	s_nop 1
	v_cndmask_b32_e32 v158, 5, v158, vcc
	v_add_u32_e32 v162, s40, v158
	v_lshl_or_b32 v162, v162, 2, v166
	v_mov_b32_e32 v163, v156
	ds_min_u64 v167, v[162:163] offset:17408
	s_waitcnt lgkmcnt(0)
	s_barrier
	s_add_i32 s65, s50, 4
	s_mov_b32 s66, 8
	s_cmp_ge_u32 s50, 2
	s_cbranch_scc0 .Lq1
	s_lshl_b32 s60, s65, 7
	v_add_u32_e32 v2, s60, v169
	ds_read_b32 v216, v2 offset:16384
	s_lshl_b32 s60, s65, 4
	v_add_u32_e32 v2, s60, v177
	v_mul_u32_u24_e32 v3, 0x556, v2
	v_lshrrev_b32_e32 v3, 16, v3
	v_mul_u32_u24_e32 v4, 48, v3
	v_sub_u32_e32 v4, v2, v4
	v_mul_u32_u24_e32 v3, 0x6c0, v3
	v_mad_u32_u24 v253, v4, 12, v3
	v_add_u32_e32 v253, v253, v175
	s_lshl_b32 s60, s65, 10
	v_add_u32_e32 v248, s60, v170
.Lq1:
	s_cmp_eq_u32 s50, 0
	s_cbranch_scc0 .Lq2
	s_lshl_b32 s60, s66, 7
	v_add_u32_e32 v2, s60, v169
	ds_read_b32 v16, v2 offset:16384
	s_lshl_b32 s60, s66, 4
	v_add_u32_e32 v2, s60, v177
	v_mul_u32_u24_e32 v3, 0x556, v2
	v_lshrrev_b32_e32 v3, 16, v3
	v_mul_u32_u24_e32 v4, 48, v3
	v_sub_u32_e32 v4, v2, v4
	v_mul_u32_u24_e32 v3, 0x6c0, v3
	v_mad_u32_u24 v53, v4, 12, v3
	v_add_u32_e32 v53, v53, v175
	s_lshl_b32 s60, s66, 10
	v_add_u32_e32 v48, s60, v170
.Lq2:
	s_waitcnt lgkmcnt(0)
	s_cmp_ge_u32 s50, 2
	s_cbranch_scc0 .Lq3
	v_lshrrev_b32_e32 v2, 2, v216
	v_mul_u32_u24_e32 v3, 43, v2
	v_lshrrev_b32_e32 v3, 8, v3
	v_mul_u32_u24_e32 v4, 6, v3
	v_sub_u32_e32 v4, v2, v4
	v_mul_u32_u24_e32 v3, 24, v3
	v_min_u32_e32 v3, 0xa5, v3
	v_lshl_add_u32 v3, v4, 2, v3
	v_lshrrev_b32_e32 v4, 2, v168
	v_add_u32_e32 v3, v3, v4
	v_and_b32_e32 v4, 3, v216
	v_lshlrev_b32_e32 v4, 2, v4
	v_and_b32_e32 v5, 3, v168
	v_or_b32_e32 v4, v4, v5
	v_lshl_or_b32 v252, v3, 4, v4
	v_add_u32_e32 v3, s9, v3
	v_lshlrev_b32_e32 v4, 4, v4
	v_lshl_or_b32 v244, v3, 10, v4
	global_load_dwordx4 v[216:219], v244, s[6:7]
	global_load_dwordx4 v[220:223], v244, s[6:7] offset:256
	global_load_dwordx4 v[224:227], v244, s[6:7] offset:512
	global_load_dwordx4 v[228:231], v244, s[6:7] offset:768
	global_load_dwordx4 v[232:235], v244, s[6:7] offset:2048
	global_load_dwordx4 v[236:239], v244, s[6:7] offset:2304
	global_load_dwordx4 v[240:243], v244, s[6:7] offset:2560
	global_load_dwordx4 v[244:247], v244, s[6:7] offset:2816
	global_load_dwordx4 v[248:251], v248, s[4:5]
.Lq3:
	s_cmp_eq_u32 s50, 0
	s_cbranch_scc0 .Lq4
	v_lshrrev_b32_e32 v2, 2, v16
	v_mul_u32_u24_e32 v3, 43, v2
	v_lshrrev_b32_e32 v3, 8, v3
	v_mul_u32_u24_e32 v4, 6, v3
	v_sub_u32_e32 v4, v2, v4
	v_mul_u32_u24_e32 v3, 24, v3
	v_min_u32_e32 v3, 0xa5, v3
	v_lshl_add_u32 v3, v4, 2, v3
	v_lshrrev_b32_e32 v4, 2, v168
	v_add_u32_e32 v3, v3, v4
	v_and_b32_e32 v4, 3, v16
	v_lshlrev_b32_e32 v4, 2, v4
	v_and_b32_e32 v5, 3, v168
	v_or_b32_e32 v4, v4, v5
	v_lshl_or_b32 v52, v3, 4, v4
	v_add_u32_e32 v3, s9, v3
	v_lshlrev_b32_e32 v4, 4, v4
	v_lshl_or_b32 v44, v3, 10, v4
	global_load_dwordx4 v[16:19], v44, s[6:7]
	global_load_dwordx4 v[20:23], v44, s[6:7] offset:256
	global_load_dwordx4 v[24:27], v44, s[6:7] offset:512
	global_load_dwordx4 v[28:31], v44, s[6:7] offset:768
	global_load_dwordx4 v[32:35], v44, s[6:7] offset:2048
	global_load_dwordx4 v[36:39], v44, s[6:7] offset:2304
	global_load_dwordx4 v[40:43], v44, s[6:7] offset:2560
	global_load_dwordx4 v[44:47], v44, s[6:7] offset:2816
	global_load_dwordx4 v[48:51], v48, s[4:5]
.Lq4:
	s_waitcnt vmcnt(9)
	v_mov_b32_e32 v56, 0
	v_mov_b32_e32 v57, 0
	v_dot2c_f32_f16_dpp v56, v210, v178 quad_perm:[0,0,0,0] row_mask:0xf bank_mask:0xf
	v_dot2c_f32_f16_dpp v57, v210, v194 quad_perm:[0,0,0,0] row_mask:0xf bank_mask:0xf
	v_dot2c_f32_f16_dpp v56, v211, v179 quad_perm:[0,0,0,0] row_mask:0xf bank_mask:0xf
	v_dot2c_f32_f16_dpp v57, v211, v195 quad_perm:[0,0,0,0] row_mask:0xf bank_mask:0xf
	v_dot2c_f32_f16_dpp v56, v212, v180 quad_perm:[0,0,0,0] row_mask:0xf bank_mask:0xf
	v_dot2c_f32_f16_dpp v57, v212, v196 quad_perm:[0,0,0,0] row_mask:0xf bank_mask:0xf
	v_dot2c_f32_f16_dpp v56, v213, v181 quad_perm:[0,0,0,0] row_mask:0xf bank_mask:0xf
	v_dot2c_f32_f16_dpp v57, v213, v197 quad_perm:[0,0,0,0] row_mask:0xf bank_mask:0xf
	v_dot2c_f32_f16_dpp v56, v210, v182 quad_perm:[1,1,1,1] row_mask:0xf bank_mask:0xf
	v_dot2c_f32_f16_dpp v57, v210, v198 quad_perm:[1,1,1,1] row_mask:0xf bank_mask:0xf
	v_dot2c_f32_f16_dpp v56, v211, v183 quad_perm:[1,1,1,1] row_mask:0xf bank_mask:0xf
	v_dot2c_f32_f16_dpp v57, v211, v199 quad_perm:[1,1,1,1] row_mask:0xf bank_mask:0xf
	v_dot2c_f32_f16_dpp v56, v212, v184 quad_perm:[1,1,1,1] row_mask:0xf bank_mask:0xf
	v_dot2c_f32_f16_dpp v57, v212, v200 quad_perm:[1,1,1,1] row_mask:0xf bank_mask:0xf
	v_dot2c_f32_f16_dpp v56, v213, v185 quad_perm:[1,1,1,1] row_mask:0xf bank_mask:0xf
	v_dot2c_f32_f16_dpp v57, v213, v201 quad_perm:[1,1,1,1] row_mask:0xf bank_mask:0xf
	v_dot2c_f32_f16_dpp v56, v210, v186 quad_perm:[2,2,2,2] row_mask:0xf bank_mask:0xf
	v_dot2c_f32_f16_dpp v57, v210, v202 quad_perm:[2,2,2,2] row_mask:0xf bank_mask:0xf
	v_dot2c_f32_f16_dpp v56, v211, v187 quad_perm:[2,2,2,2] row_mask:0xf bank_mask:0xf
	v_dot2c_f32_f16_dpp v57, v211, v203 quad_perm:[2,2,2,2] row_mask:0xf bank_mask:0xf
	v_dot2c_f32_f16_dpp v56, v212, v188 quad_perm:[2,2,2,2] row_mask:0xf bank_mask:0xf
	v_dot2c_f32_f16_dpp v57, v212, v204 quad_perm:[2,2,2,2] row_mask:0xf bank_mask:0xf
	v_dot2c_f32_f16_dpp v56, v213, v189 quad_perm:[2,2,2,2] row_mask:0xf bank_mask:0xf
	v_dot2c_f32_f16_dpp v57, v213, v205 quad_perm:[2,2,2,2] row_mask:0xf bank_mask:0xf
	v_dot2c_f32_f16_dpp v56, v210, v190 quad_perm:[3,3,3,3] row_mask:0xf bank_mask:0xf
	v_dot2c_f32_f16_dpp v57, v210, v206 quad_perm:[3,3,3,3] row_mask:0xf bank_mask:0xf
	v_dot2c_f32_f16_dpp v56, v211, v191 quad_perm:[3,3,3,3] row_mask:0xf bank_mask:0xf
	v_dot2c_f32_f16_dpp v57, v211, v207 quad_perm:[3,3,3,3] row_mask:0xf bank_mask:0xf
	v_dot2c_f32_f16_dpp v56, v212, v192 quad_perm:[3,3,3,3] row_mask:0xf bank_mask:0xf
	v_dot2c_f32_f16_dpp v57, v212, v208 quad_perm:[3,3,3,3] row_mask:0xf bank_mask:0xf
	v_dot2c_f32_f16_dpp v56, v213, v193 quad_perm:[3,3,3,3] row_mask:0xf bank_mask:0xf
	v_dot2c_f32_f16_dpp v57, v213, v209 quad_perm:[3,3,3,3] row_mask:0xf bank_mask:0xf
	s_nop 2
	v_and_or_b32 v2, v56, -16, v168
	v_and_or_b32 v3, v57, -16, v176
	v_min_i32_e32 v58, v2, v3
	s_nop 1
	v_min_i32_dpp v58, v58, v58 quad_perm:[1,0,3,2] row_mask:0xf bank_mask:0xf bound_ctrl:1
	s_nop 1
	v_min_i32_dpp v58, v58, v58 quad_perm:[2,3,0,1] row_mask:0xf bank_mask:0xf bound_ctrl:1
	s_nop 1
	v_min_i32_dpp v58, v58, v58 row_half_mirror row_mask:0xf bank_mask:0xf bound_ctrl:1
	v_and_b32_e32 v2, 12, v58
	v_lshlrev_b32_e32 v2, 2, v2
	v_and_b32_e32 v3, 3, v58
	v_sub_u32_e32 v4, v214, v171
	v_add3_u32 v59, v4, v2, v3
	v_cmp_le_u32_e64 s[54:55], s58, v59
	v_cmp_le_u32_e64 s[56:57], s59, v59
	s_nop 1
	v_cndmask_b32_e64 v2, 0, v7, s[54:55]
	v_cndmask_b32_e64 v3, 0, v8, s[56:57]
	v_sub_u32_e32 v4, v59, v2
	v_sub_u32_e32 v4, v4, v3
	v_cndmask_b32_e64 v2, 0, 1, s[54:55]
	v_cndmask_b32_e64 v3, 0, 1, s[56:57]
	v_add_u32_e32 v5, v2, v3
	v_lshlrev_b32_e32 v2, v5, v4
	v_mul_u32_u24_e32 v2, 0xaab, v2
	v_lshrrev_b32_e32 v2, 17, v2
	v_mul_u32_u24_e32 v3, 0x60, v2
	v_lshrrev_b32_e32 v3, v5, v3
	v_add_u32_e32 v3, v4, v3
	v_mul_u32_u24_e32 v3, 12, v3
	v_cndmask_b32_e64 v2, v172, v173, s[54:55]
	v_cndmask_b32_e64 v2, v2, v174, s[56:57]
	v_add_u32_e32 v3, v3, v2
	v_cndmask_b32_e64 v2, v152, v154, s[54:55]
	v_cndmask_b32_e64 v2, v2, v159, s[56:57]
	v_cndmask_b32_e64 v4, v153, v155, s[54:55]
	v_cndmask_b32_e64 v4, v4, v161, s[56:57]
	v_add_co_u32_e64 v60, s[60:61], v2, v3
	s_nop 1
	v_addc_co_u32_e64 v61, s[60:61], 0, v4, s[60:61]
	v_sub_u32_e32 v2, 2, v5
	v_lshlrev_b32_e64 v2, v2, 36
	v_add_u32_e32 v4, 1, v2
	v_mul_u32_u24_e32 v2, v2, v4
	v_lshlrev_b32_e32 v2, 3, v2
	v_add_co_u32_e64 v62, s[60:61], v60, v2
	s_nop 1
	v_addc_co_u32_e64 v63, s[60:61], 0, v61, s[60:61]
	global_load_dwordx3 v[64:66], v[60:61], off
	ds_read_b32 v72, v215
	ds_read_b32 v73, v215 offset:4
	ds_read_b32 v74, v215 offset:8
	s_mov_b64 s[52:53], exec
	s_and_b64 exec, exec, s[48:49]
	global_load_dwordx3 v[68:70], v[62:63], off
	ds_read_b32 v76, v215 offset:11520
	ds_read_b32 v77, v215 offset:11524
	ds_read_b32 v78, v215 offset:11528
	s_mov_b64 exec, s[52:53]
	s_waitcnt vmcnt(2)
	v_mov_b32_e32 v84, 0
	v_mov_b32_e32 v85, 0
	v_dot2c_f32_f16_dpp v84, v248, v216 quad_perm:[0,0,0,0] row_mask:0xf bank_mask:0xf
	v_dot2c_f32_f16_dpp v85, v248, v232 quad_perm:[0,0,0,0] row_mask:0xf bank_mask:0xf
	v_dot2c_f32_f16_dpp v84, v249, v217 quad_perm:[0,0,0,0] row_mask:0xf bank_mask:0xf
	v_dot2c_f32_f16_dpp v85, v249, v233 quad_perm:[0,0,0,0] row_mask:0xf bank_mask:0xf
	v_dot2c_f32_f16_dpp v84, v250, v218 quad_perm:[0,0,0,0] row_mask:0xf bank_mask:0xf
	v_dot2c_f32_f16_dpp v85, v250, v234 quad_perm:[0,0,0,0] row_mask:0xf bank_mask:0xf
	v_dot2c_f32_f16_dpp v84, v251, v219 quad_perm:[0,0,0,0] row_mask:0xf bank_mask:0xf
	v_dot2c_f32_f16_dpp v85, v251, v235 quad_perm:[0,0,0,0] row_mask:0xf bank_mask:0xf
	v_dot2c_f32_f16_dpp v84, v248, v220 quad_perm:[1,1,1,1] row_mask:0xf bank_mask:0xf
	v_dot2c_f32_f16_dpp v85, v248, v236 quad_perm:[1,1,1,1] row_mask:0xf bank_mask:0xf
	v_dot2c_f32_f16_dpp v84, v249, v221 quad_perm:[1,1,1,1] row_mask:0xf bank_mask:0xf
	v_dot2c_f32_f16_dpp v85, v249, v237 quad_perm:[1,1,1,1] row_mask:0xf bank_mask:0xf
	v_dot2c_f32_f16_dpp v84, v250, v222 quad_perm:[1,1,1,1] row_mask:0xf bank_mask:0xf
	v_dot2c_f32_f16_dpp v85, v250, v238 quad_perm:[1,1,1,1] row_mask:0xf bank_mask:0xf
	v_dot2c_f32_f16_dpp v84, v251, v223 quad_perm:[1,1,1,1] row_mask:0xf bank_mask:0xf
	v_dot2c_f32_f16_dpp v85, v251, v239 quad_perm:[1,1,1,1] row_mask:0xf bank_mask:0xf
	v_dot2c_f32_f16_dpp v84, v248, v224 quad_perm:[2,2,2,2] row_mask:0xf bank_mask:0xf
	v_dot2c_f32_f16_dpp v85, v248, v240 quad_perm:[2,2,2,2] row_mask:0xf bank_mask:0xf
	v_dot2c_f32_f16_dpp v84, v249, v225 quad_perm:[2,2,2,2] row_mask:0xf bank_mask:0xf
	v_dot2c_f32_f16_dpp v85, v249, v241 quad_perm:[2,2,2,2] row_mask:0xf bank_mask:0xf
	v_dot2c_f32_f16_dpp v84, v250, v226 quad_perm:[2,2,2,2] row_mask:0xf bank_mask:0xf
	v_dot2c_f32_f16_dpp v85, v250, v242 quad_perm:[2,2,2,2] row_mask:0xf bank_mask:0xf
	v_dot2c_f32_f16_dpp v84, v251, v227 quad_perm:[2,2,2,2] row_mask:0xf bank_mask:0xf
	v_dot2c_f32_f16_dpp v85, v251, v243 quad_perm:[2,2,2,2] row_mask:0xf bank_mask:0xf
	v_dot2c_f32_f16_dpp v84, v248, v228 quad_perm:[3,3,3,3] row_mask:0xf bank_mask:0xf
	v_dot2c_f32_f16_dpp v85, v248, v244 quad_perm:[3,3,3,3] row_mask:0xf bank_mask:0xf
	v_dot2c_f32_f16_dpp v84, v249, v229 quad_perm:[3,3,3,3] row_mask:0xf bank_mask:0xf
	v_dot2c_f32_f16_dpp v85, v249, v245 quad_perm:[3,3,3,3] row_mask:0xf bank_mask:0xf
	v_dot2c_f32_f16_dpp v84, v250, v230 quad_perm:[3,3,3,3] row_mask:0xf bank_mask:0xf
	v_dot2c_f32_f16_dpp v85, v250, v246 quad_perm:[3,3,3,3] row_mask:0xf bank_mask:0xf
	v_dot2c_f32_f16_dpp v84, v251, v231 quad_perm:[3,3,3,3] row_mask:0xf bank_mask:0xf
	v_dot2c_f32_f16_dpp v85, v251, v247 quad_perm:[3,3,3,3] row_mask:0xf bank_mask:0xf
	s_nop 2
	v_and_or_b32 v2, v84, -16, v168
	v_and_or_b32 v3, v85, -16, v176
	v_min_i32_e32 v86, v2, v3
	s_nop 1
	v_min_i32_dpp v86, v86, v86 quad_perm:[1,0,3,2] row_mask:0xf bank_mask:0xf bound_ctrl:1
	s_nop 1
	v_min_i32_dpp v86, v86, v86 quad_perm:[2,3,0,1] row_mask:0xf bank_mask:0xf bound_ctrl:1
	s_nop 1
	v_min_i32_dpp v86, v86, v86 row_half_mirror row_mask:0xf bank_mask:0xf bound_ctrl:1
	v_and_b32_e32 v2, 12, v86
	v_lshlrev_b32_e32 v2, 2, v2
	v_and_b32_e32 v3, 3, v86
	v_sub_u32_e32 v4, v252, v171
	v_add3_u32 v87, v4, v2, v3
	v_cmp_le_u32_e64 s[54:55], s58, v87
	v_cmp_le_u32_e64 s[56:57], s59, v87
	s_nop 1
	v_cndmask_b32_e64 v2, 0, v7, s[54:55]
	v_cndmask_b32_e64 v3, 0, v8, s[56:57]
	v_sub_u32_e32 v4, v87, v2
	v_sub_u32_e32 v4, v4, v3
	v_cndmask_b32_e64 v2, 0, 1, s[54:55]
	v_cndmask_b32_e64 v3, 0, 1, s[56:57]
	v_add_u32_e32 v5, v2, v3
	v_lshlrev_b32_e32 v2, v5, v4
	v_mul_u32_u24_e32 v2, 0xaab, v2
	v_lshrrev_b32_e32 v2, 17, v2
	v_mul_u32_u24_e32 v3, 0x60, v2
	v_lshrrev_b32_e32 v3, v5, v3
	v_add_u32_e32 v3, v4, v3
	v_mul_u32_u24_e32 v3, 12, v3
	v_cndmask_b32_e64 v2, v172, v173, s[54:55]
	v_cndmask_b32_e64 v2, v2, v174, s[56:57]
	v_add_u32_e32 v3, v3, v2
	v_cndmask_b32_e64 v2, v152, v154, s[54:55]
	v_cndmask_b32_e64 v2, v2, v159, s[56:57]
	v_cndmask_b32_e64 v4, v153, v155, s[54:55]
	v_cndmask_b32_e64 v4, v4, v161, s[56:57]
	v_add_co_u32_e64 v88, s[60:61], v2, v3
	s_nop 1
	v_addc_co_u32_e64 v89, s[60:61], 0, v4, s[60:61]
	v_sub_u32_e32 v2, 2, v5
	v_lshlrev_b32_e64 v2, v2, 36
	v_add_u32_e32 v4, 1, v2
	v_mul_u32_u24_e32 v2, v2, v4
	v_lshlrev_b32_e32 v2, 3, v2
	v_add_co_u32_e64 v90, s[60:61], v88, v2
	s_nop 1
	v_addc_co_u32_e64 v91, s[60:61], 0, v89, s[60:61]
	global_load_dwordx3 v[92:94], v[88:89], off
	ds_read_b32 v100, v253
	ds_read_b32 v101, v253 offset:4
	ds_read_b32 v102, v253 offset:8
	s_mov_b64 s[52:53], exec
	s_and_b64 exec, exec, s[48:49]
	global_load_dwordx3 v[96:98], v[90:91], off
	ds_read_b32 v104, v253 offset:11520
	ds_read_b32 v105, v253 offset:11524
	ds_read_b32 v106, v253 offset:11528
	s_mov_b64 exec, s[52:53]
	s_cmp_eq_u32 s50, 0
	s_cbranch_scc0 .Lq5
	s_waitcnt vmcnt(4)
	v_mov_b32_e32 v112, 0
	v_mov_b32_e32 v113, 0
	v_dot2c_f32_f16_dpp v112, v48, v16 quad_perm:[0,0,0,0] row_mask:0xf bank_mask:0xf
	v_dot2c_f32_f16_dpp v113, v48, v32 quad_perm:[0,0,0,0] row_mask:0xf bank_mask:0xf
	v_dot2c_f32_f16_dpp v112, v49, v17 quad_perm:[0,0,0,0] row_mask:0xf bank_mask:0xf
	v_dot2c_f32_f16_dpp v113, v49, v33 quad_perm:[0,0,0,0] row_mask:0xf bank_mask:0xf
	v_dot2c_f32_f16_dpp v112, v50, v18 quad_perm:[0,0,0,0] row_mask:0xf bank_mask:0xf
	v_dot2c_f32_f16_dpp v113, v50, v34 quad_perm:[0,0,0,0] row_mask:0xf bank_mask:0xf
	v_dot2c_f32_f16_dpp v112, v51, v19 quad_perm:[0,0,0,0] row_mask:0xf bank_mask:0xf
	v_dot2c_f32_f16_dpp v113, v51, v35 quad_perm:[0,0,0,0] row_mask:0xf bank_mask:0xf
	v_dot2c_f32_f16_dpp v112, v48, v20 quad_perm:[1,1,1,1] row_mask:0xf bank_mask:0xf
	v_dot2c_f32_f16_dpp v113, v48, v36 quad_perm:[1,1,1,1] row_mask:0xf bank_mask:0xf
	v_dot2c_f32_f16_dpp v112, v49, v21 quad_perm:[1,1,1,1] row_mask:0xf bank_mask:0xf
	v_dot2c_f32_f16_dpp v113, v49, v37 quad_perm:[1,1,1,1] row_mask:0xf bank_mask:0xf
	v_dot2c_f32_f16_dpp v112, v50, v22 quad_perm:[1,1,1,1] row_mask:0xf bank_mask:0xf
	v_dot2c_f32_f16_dpp v113, v50, v38 quad_perm:[1,1,1,1] row_mask:0xf bank_mask:0xf
	v_dot2c_f32_f16_dpp v112, v51, v23 quad_perm:[1,1,1,1] row_mask:0xf bank_mask:0xf
	v_dot2c_f32_f16_dpp v113, v51, v39 quad_perm:[1,1,1,1] row_mask:0xf bank_mask:0xf
	v_dot2c_f32_f16_dpp v112, v48, v24 quad_perm:[2,2,2,2] row_mask:0xf bank_mask:0xf
	v_dot2c_f32_f16_dpp v113, v48, v40 quad_perm:[2,2,2,2] row_mask:0xf bank_mask:0xf
	v_dot2c_f32_f16_dpp v112, v49, v25 quad_perm:[2,2,2,2] row_mask:0xf bank_mask:0xf
	v_dot2c_f32_f16_dpp v113, v49, v41 quad_perm:[2,2,2,2] row_mask:0xf bank_mask:0xf
	v_dot2c_f32_f16_dpp v112, v50, v26 quad_perm:[2,2,2,2] row_mask:0xf bank_mask:0xf
	v_dot2c_f32_f16_dpp v113, v50, v42 quad_perm:[2,2,2,2] row_mask:0xf bank_mask:0xf
	v_dot2c_f32_f16_dpp v112, v51, v27 quad_perm:[2,2,2,2] row_mask:0xf bank_mask:0xf
	v_dot2c_f32_f16_dpp v113, v51, v43 quad_perm:[2,2,2,2] row_mask:0xf bank_mask:0xf
	v_dot2c_f32_f16_dpp v112, v48, v28 quad_perm:[3,3,3,3] row_mask:0xf bank_mask:0xf
	v_dot2c_f32_f16_dpp v113, v48, v44 quad_perm:[3,3,3,3] row_mask:0xf bank_mask:0xf
	v_dot2c_f32_f16_dpp v112, v49, v29 quad_perm:[3,3,3,3] row_mask:0xf bank_mask:0xf
	v_dot2c_f32_f16_dpp v113, v49, v45 quad_perm:[3,3,3,3] row_mask:0xf bank_mask:0xf
	v_dot2c_f32_f16_dpp v112, v50, v30 quad_perm:[3,3,3,3] row_mask:0xf bank_mask:0xf
	v_dot2c_f32_f16_dpp v113, v50, v46 quad_perm:[3,3,3,3] row_mask:0xf bank_mask:0xf
	v_dot2c_f32_f16_dpp v112, v51, v31 quad_perm:[3,3,3,3] row_mask:0xf bank_mask:0xf
	v_dot2c_f32_f16_dpp v113, v51, v47 quad_perm:[3,3,3,3] row_mask:0xf bank_mask:0xf
	s_nop 2
	v_and_or_b32 v2, v112, -16, v168
	v_and_or_b32 v3, v113, -16, v176
	v_min_i32_e32 v114, v2, v3
	s_nop 1
	v_min_i32_dpp v114, v114, v114 quad_perm:[1,0,3,2] row_mask:0xf bank_mask:0xf bound_ctrl:1
	s_nop 1
	v_min_i32_dpp v114, v114, v114 quad_perm:[2,3,0,1] row_mask:0xf bank_mask:0xf bound_ctrl:1
	s_nop 1
	v_min_i32_dpp v114, v114, v114 row_half_mirror row_mask:0xf bank_mask:0xf bound_ctrl:1
	v_and_b32_e32 v2, 12, v114
	v_lshlrev_b32_e32 v2, 2, v2
	v_and_b32_e32 v3, 3, v114
	v_sub_u32_e32 v4, v52, v171
	v_add3_u32 v115, v4, v2, v3
	v_cmp_le_u32_e64 s[54:55], s58, v115
	v_cmp_le_u32_e64 s[56:57], s59, v115
	s_nop 1
	v_cndmask_b32_e64 v2, 0, v7, s[54:55]
	v_cndmask_b32_e64 v3, 0, v8, s[56:57]
	v_sub_u32_e32 v4, v115, v2
	v_sub_u32_e32 v4, v4, v3
	v_cndmask_b32_e64 v2, 0, 1, s[54:55]
	v_cndmask_b32_e64 v3, 0, 1, s[56:57]
	v_add_u32_e32 v5, v2, v3
	v_lshlrev_b32_e32 v2, v5, v4
	v_mul_u32_u24_e32 v2, 0xaab, v2
	v_lshrrev_b32_e32 v2, 17, v2
	v_mul_u32_u24_e32 v3, 0x60, v2
	v_lshrrev_b32_e32 v3, v5, v3
	v_add_u32_e32 v3, v4, v3
	v_mul_u32_u24_e32 v3, 12, v3
	v_cndmask_b32_e64 v2, v172, v173, s[54:55]
	v_cndmask_b32_e64 v2, v2, v174, s[56:57]
	v_add_u32_e32 v3, v3, v2
	v_cndmask_b32_e64 v2, v152, v154, s[54:55]
	v_cndmask_b32_e64 v2, v2, v159, s[56:57]
	v_cndmask_b32_e64 v4, v153, v155, s[54:55]
	v_cndmask_b32_e64 v4, v4, v161, s[56:57]
	v_add_co_u32_e64 v116, s[60:61], v2, v3
	s_nop 1
	v_addc_co_u32_e64 v117, s[60:61], 0, v4, s[60:61]
	v_sub_u32_e32 v2, 2, v5
	v_lshlrev_b32_e64 v2, v2, 36
	v_add_u32_e32 v4, 1, v2
	v_mul_u32_u24_e32 v2, v2, v4
	v_lshlrev_b32_e32 v2, 3, v2
	v_add_co_u32_e64 v118, s[60:61], v116, v2
	s_nop 1
	v_addc_co_u32_e64 v119, s[60:61], 0, v117, s[60:61]
	global_load_dwordx3 v[120:122], v[116:117], off
	ds_read_b32 v128, v53
	ds_read_b32 v129, v53 offset:4
	ds_read_b32 v130, v53 offset:8
	s_mov_b64 s[52:53], exec
	s_and_b64 exec, exec, s[48:49]
	global_load_dwordx3 v[124:126], v[118:119], off
	ds_read_b32 v132, v53 offset:11520
	ds_read_b32 v133, v53 offset:11524
	ds_read_b32 v134, v53 offset:11528
	s_mov_b64 exec, s[52:53]
.Lq5:
	s_waitcnt vmcnt(2)
	s_waitcnt lgkmcnt(0)
	v_sub_f32_e32 v2, v72, v64
	v_add_f32_e64 v6, v6, |v2|
	v_sub_f32_e32 v2, v73, v65
	v_add_f32_e64 v6, v6, |v2|
	v_sub_f32_e32 v2, v74, v66
	v_add_f32_e64 v6, v6, |v2|
	s_mov_b64 s[52:53], exec
	s_and_b64 exec, exec, s[48:49]
	v_sub_f32_e32 v2, v76, v68
	v_add_f32_e64 v6, v6, |v2|
	v_sub_f32_e32 v2, v77, v69
	v_add_f32_e64 v6, v6, |v2|
	v_sub_f32_e32 v2, v78, v70
	v_add_f32_e64 v6, v6, |v2|
	s_mov_b64 exec, s[52:53]
	s_waitcnt vmcnt(0)
	s_waitcnt lgkmcnt(0)
	v_sub_f32_e32 v2, v100, v92
	v_add_f32_e64 v6, v6, |v2|
	v_sub_f32_e32 v2, v101, v93
	v_add_f32_e64 v6, v6, |v2|
	v_sub_f32_e32 v2, v102, v94
	v_add_f32_e64 v6, v6, |v2|
	s_mov_b64 s[52:53], exec
	s_and_b64 exec, exec, s[48:49]
	v_sub_f32_e32 v2, v104, v96
	v_add_f32_e64 v6, v6, |v2|
	v_sub_f32_e32 v2, v105, v97
	v_add_f32_e64 v6, v6, |v2|
	v_sub_f32_e32 v2, v106, v98
	v_add_f32_e64 v6, v6, |v2|
	s_mov_b64 exec, s[52:53]
	s_cmp_eq_u32 s50, 0
	s_cbranch_scc0 .Lq6
	s_waitcnt lgkmcnt(0)
	v_sub_f32_e32 v2, v128, v120
	v_add_f32_e64 v6, v6, |v2|
	v_sub_f32_e32 v2, v129, v121
	v_add_f32_e64 v6, v6, |v2|
	v_sub_f32_e32 v2, v130, v122
	v_add_f32_e64 v6, v6, |v2|
	s_mov_b64 s[52:53], exec
	s_and_b64 exec, exec, s[48:49]
	v_sub_f32_e32 v2, v132, v124
	v_add_f32_e64 v6, v6, |v2|
	v_sub_f32_e32 v2, v133, v125
	v_add_f32_e64 v6, v6, |v2|
	v_sub_f32_e32 v2, v134, v126
	v_add_f32_e64 v6, v6, |v2|
	s_mov_b64 exec, s[52:53]
.Lq6:
	s_nop 1
	v_add_f32_dpp v6, v6, v6 quad_perm:[1,0,3,2] row_mask:0xf bank_mask:0xf
	s_nop 1
	v_add_f32_dpp v6, v6, v6 quad_perm:[2,3,0,1] row_mask:0xf bank_mask:0xf
	s_nop 1
	v_add_f32_dpp v6, v6, v6 row_half_mirror row_mask:0xf bank_mask:0xf
	s_nop 1
	v_add_f32_dpp v6, v6, v6 row_mirror row_mask:0xf bank_mask:0xf
	s_nop 1
	v_add_f32_dpp v6, v6, v6 row_bcast:15 row_mask:0xa bank_mask:0xf
	s_nop 1
	v_add_f32_dpp v6, v6, v6 row_bcast:31 row_mask:0xc bank_mask:0xf
	s_lshl_b32 s60, s15, 2
	v_mov_b32_e32 v2, s60
	s_mov_b64 s[52:53], exec
	s_mov_b32 exec_lo, 0
	s_mov_b32 exec_hi, 0x80000000
	ds_write_b32 v2, v6 offset:18112
	s_mov_b64 exec, s[52:53]
	s_load_dwordx2 s[2:3], s[0:1], 0x18
	v_cmp_eq_u32_e32 vcc, 0, v0
	s_waitcnt lgkmcnt(0)
	s_barrier
	s_and_saveexec_b64 s[0:1], vcc
	s_cbranch_execz .LBB1_34
	v_mov_b32_e32 v0, 0
	ds_read_b128 v[2:5], v0 offset:18112
	ds_read_b128 v[6:9], v0 offset:18128
	s_mov_b64 s[6:7], exec
	s_waitcnt lgkmcnt(0)
	v_add_f32_e32 v1, v2, v3
	v_add_f32_e32 v1, v1, v4
	v_add_f32_e32 v1, v1, v5
	v_add_f32_e32 v1, v1, v6
	v_add_f32_e32 v1, v1, v7
	v_add_f32_e32 v1, v1, v8
	v_add_f32_e32 v1, v1, v9
	v_mul_f32_e32 v1, 0x49800000, v1
	v_cvt_u32_f32_e32 v2, v1
	v_mbcnt_lo_u32_b32 v1, s6, 0
	v_mbcnt_hi_u32_b32 v1, s7, v1
	v_cmp_eq_u32_e32 vcc, 0, v1
	s_and_saveexec_b64 s[0:1], vcc
	s_cbranch_execz .LBB1_27
	s_lshl_b32 s8, s14, 4
	s_ashr_i32 s9, s8, 31
	s_lshl_b64 s[8:9], s[8:9], 3
	s_add_u32 s8, s4, s8
	s_addc_u32 s9, s5, s9
	s_bcnt1_i32_b64 s6, s[6:7]
	v_mov_b32_e32 v3, 0x1000000
	v_mul_lo_u32 v3, v3, s6
	v_mul_hi_u32 v4, v2, s6
	v_add_u32_e32 v5, v4, v3
	v_mul_lo_u32 v4, v2, s6
	v_mov_b32_e32 v3, 0x663000
	global_atomic_add_x2 v[4:5], v3, v[4:5], s[8:9] offset:3072 sc0
